# GEMM K-loops: adjacent s_setprio 0/1 pairs between MFMA groups removed
# speedup vs baseline: 1.0045x; 1.0045x over previous
.LBB0_162:
	s_setprio 0
	s_barrier
	s_add_i32 s56, 0, 0x18000
	s_add_i32 s57, 0, 0x1c000
	v_add_u32_e32 v2, s56, v234
	v_add_u32_e32 v22, s57, v234
	ds_read_b128 v[10:13], v2
	ds_read_b128 v[14:17], v2 offset:1024
	ds_read_b128 v[26:29], v2 offset:2048
	ds_read_b128 v[30:33], v2 offset:3072
	ds_read_b128 v[2:5], v22
	ds_read_b128 v[6:9], v22 offset:1024
	ds_read_b128 v[18:21], v22 offset:2048
	ds_read_b128 v[22:25], v22 offset:3072
	s_add_u32 s54, s54, 0x20000
	s_addc_u32 s55, s55, 0
	s_mov_b32 m0, s68
	v_lshl_add_u64 v[218:219], s[54:55], 0, v[194:195]
	s_waitcnt lgkmcnt(0)
	ds_read_b128 v[34:37], v238 offset:32768
	ds_read_b128 v[38:41], v238 offset:33792
	ds_read_b128 v[42:45], v238 offset:34816
	ds_read_b128 v[46:49], v238 offset:35840
	ds_read_b128 v[50:53], v238 offset:36864
	ds_read_b128 v[54:57], v238 offset:37888
	ds_read_b128 v[58:61], v238 offset:38912
	ds_read_b128 v[62:65], v238 offset:39936
	global_load_lds_dwordx4 v[218:219], off
	v_lshl_add_u64 v[218:219], s[54:55], 0, v[198:199]
	s_mov_b32 m0, s69
	s_nop 0
	global_load_lds_dwordx4 v[218:219], off
	s_waitcnt vmcnt(8)
	s_waitcnt lgkmcnt(0)
	s_barrier
	s_setprio 1
	s_waitcnt lgkmcnt(0)
	v_mfma_scale_f32_16x16x128_f8f6f4 v[106:109], v[10:17], v[34:41], v[106:109], v236, v237 op_sel_hi:[0,0,0]
	v_mfma_scale_f32_16x16x128_f8f6f4 v[122:125], v[26:33], v[34:41], v[122:125], v236, v237 op_sel_hi:[0,0,0]
	v_mfma_scale_f32_16x16x128_f8f6f4 v[134:137], v[10:17], v[42:49], v[134:137], v236, v237 op_sel_hi:[0,0,0]
	v_mfma_scale_f32_16x16x128_f8f6f4 v[146:149], v[26:33], v[42:49], v[146:149], v236, v237 op_sel_hi:[0,0,0]
	v_mfma_scale_f32_16x16x128_f8f6f4 v[158:161], v[10:17], v[50:57], v[158:161], v236, v237 op_sel_hi:[0,0,0]
	v_mfma_scale_f32_16x16x128_f8f6f4 v[114:117], v[26:33], v[50:57], v[114:117], v236, v237 op_sel_hi:[0,0,0]
	v_mfma_scale_f32_16x16x128_f8f6f4 v[126:129], v[10:17], v[58:65], v[126:129], v236, v237 op_sel_hi:[0,0,0]
	v_mfma_scale_f32_16x16x128_f8f6f4 v[138:141], v[26:33], v[58:65], v[138:141], v236, v237 op_sel_hi:[0,0,0]
	v_mfma_scale_f32_16x16x128_f8f6f4 v[162:165], v[2:9], v[34:41], v[162:165], v236, v237 op_sel_hi:[0,0,0]
	v_mfma_scale_f32_16x16x128_f8f6f4 v[166:169], v[18:25], v[34:41], v[166:169], v236, v237 op_sel_hi:[0,0,0]
	v_mfma_scale_f32_16x16x128_f8f6f4 v[170:173], v[2:9], v[42:49], v[170:173], v236, v237 op_sel_hi:[0,0,0]
	v_mfma_scale_f32_16x16x128_f8f6f4 v[174:177], v[18:25], v[42:49], v[174:177], v236, v237 op_sel_hi:[0,0,0]
	v_mfma_scale_f32_16x16x128_f8f6f4 v[178:181], v[2:9], v[50:57], v[178:181], v236, v237 op_sel_hi:[0,0,0]
	v_mfma_scale_f32_16x16x128_f8f6f4 v[182:185], v[18:25], v[50:57], v[182:185], v236, v237 op_sel_hi:[0,0,0]
	v_mfma_scale_f32_16x16x128_f8f6f4 v[186:189], v[2:9], v[58:65], v[186:189], v236, v237 op_sel_hi:[0,0,0]
	v_mfma_scale_f32_16x16x128_f8f6f4 v[190:193], v[18:25], v[58:65], v[190:193], v236, v237 op_sel_hi:[0,0,0]
	s_setprio 0
	s_barrier
	s_add_i32 s54, s56, s61
	v_lshl_add_u64 v[216:217], v[216:217], 0, s[16:17]
	s_mov_b32 m0, s54
	ds_read_b128 v[34:37], v238 offset:49152
	ds_read_b128 v[38:41], v238 offset:50176
	ds_read_b128 v[42:45], v238 offset:51200
	ds_read_b128 v[46:49], v238 offset:52224
	ds_read_b128 v[50:53], v238 offset:53248
	ds_read_b128 v[54:57], v238 offset:54272
	ds_read_b128 v[58:61], v238 offset:55296
	ds_read_b128 v[62:65], v238 offset:56320
	global_load_lds_dwordx4 v[216:217], off
	s_add_i32 m0, s54, 0x2000
	s_add_u32 s52, s52, 0x20080
	v_lshl_add_u64 v[214:215], v[214:215], 0, s[16:17]
	s_addc_u32 s53, s53, 0
	s_add_i32 s54, s57, s61
	global_load_lds_dwordx4 v[214:215], off
	v_lshl_add_u64 v[214:215], s[52:53], 0, v[196:197]
	s_mov_b32 m0, s54
	v_lshl_add_u64 v[210:211], v[210:211], 0, s[16:17]
	global_load_lds_dwordx4 v[214:215], off
	v_lshl_add_u64 v[214:215], s[52:53], 0, v[200:201]
	s_add_i32 m0, s54, 0x2000
	s_nop 0
	global_load_lds_dwordx4 v[214:215], off
	s_mov_b32 m0, s88
	s_nop 0
	global_load_lds_dwordx4 v[210:211], off
	v_lshl_add_u64 v[210:211], v[212:213], 0, s[16:17]
	s_mov_b32 m0, s89
	s_nop 0
	global_load_lds_dwordx4 v[210:211], off
	s_waitcnt vmcnt(8)
	s_waitcnt lgkmcnt(0)
	s_barrier
	s_setprio 1
	s_waitcnt lgkmcnt(0)
	v_mfma_scale_f32_16x16x128_f8f6f4 v[66:69], v[10:17], v[34:41], v[66:69], v236, v237 op_sel_hi:[0,0,0]
	v_mfma_scale_f32_16x16x128_f8f6f4 v[70:73], v[26:33], v[34:41], v[70:73], v236, v237 op_sel_hi:[0,0,0]
	v_mfma_scale_f32_16x16x128_f8f6f4 v[74:77], v[10:17], v[42:49], v[74:77], v236, v237 op_sel_hi:[0,0,0]
	v_mfma_scale_f32_16x16x128_f8f6f4 v[78:81], v[26:33], v[42:49], v[78:81], v236, v237 op_sel_hi:[0,0,0]
	v_mfma_scale_f32_16x16x128_f8f6f4 v[82:85], v[10:17], v[50:57], v[82:85], v236, v237 op_sel_hi:[0,0,0]
	v_mfma_scale_f32_16x16x128_f8f6f4 v[86:89], v[26:33], v[50:57], v[86:89], v236, v237 op_sel_hi:[0,0,0]
	v_mfma_scale_f32_16x16x128_f8f6f4 v[90:93], v[10:17], v[58:65], v[90:93], v236, v237 op_sel_hi:[0,0,0]
	v_mfma_scale_f32_16x16x128_f8f6f4 v[94:97], v[26:33], v[58:65], v[94:97], v236, v237 op_sel_hi:[0,0,0]
	v_mfma_scale_f32_16x16x128_f8f6f4 v[98:101], v[2:9], v[34:41], v[98:101], v236, v237 op_sel_hi:[0,0,0]
	v_mfma_scale_f32_16x16x128_f8f6f4 v[102:105], v[18:25], v[34:41], v[102:105], v236, v237 op_sel_hi:[0,0,0]
	v_mfma_scale_f32_16x16x128_f8f6f4 v[110:113], v[2:9], v[42:49], v[110:113], v236, v237 op_sel_hi:[0,0,0]
	v_mfma_scale_f32_16x16x128_f8f6f4 v[118:121], v[18:25], v[42:49], v[118:121], v236, v237 op_sel_hi:[0,0,0]
	v_mfma_scale_f32_16x16x128_f8f6f4 v[130:133], v[2:9], v[50:57], v[130:133], v236, v237 op_sel_hi:[0,0,0]
	v_mfma_scale_f32_16x16x128_f8f6f4 v[142:145], v[18:25], v[50:57], v[142:145], v236, v237 op_sel_hi:[0,0,0]
	v_mfma_scale_f32_16x16x128_f8f6f4 v[150:153], v[2:9], v[58:65], v[150:153], v236, v237 op_sel_hi:[0,0,0]
	v_mfma_scale_f32_16x16x128_f8f6f4 v[154:157], v[18:25], v[58:65], v[154:157], v236, v237 op_sel_hi:[0,0,0]
	s_setprio 0
	s_barrier
	s_add_i32 s78, s78, 2
	s_add_u32 s46, s46, 0x100
	s_addc_u32 s47, s47, 0
	s_cmp_gt_u32 s78, 5
	s_cbranch_scc1 .LBB0_171
.LBB0_163:
	v_add_u32_e32 v10, 0, v234
	v_add_u32_e32 v11, 0x10000, v10
	v_add_u32_e32 v30, 0x14000, v10
	ds_read_b128 v[2:5], v11
	ds_read_b128 v[6:9], v11 offset:1024
	ds_read_b128 v[18:21], v11 offset:2048
	ds_read_b128 v[22:25], v11 offset:3072
	ds_read_b128 v[10:13], v30
	ds_read_b128 v[14:17], v30 offset:1024
	ds_read_b128 v[26:29], v30 offset:2048
	ds_read_b128 v[30:33], v30 offset:3072
	v_lshl_add_u64 v[210:211], v[206:207], 0, s[46:47]
	s_add_i32 m0, s62, 0xc000
	ds_read_b128 v[34:37], v238
	ds_read_b128 v[38:41], v238 offset:1024
	ds_read_b128 v[42:45], v238 offset:2048
	ds_read_b128 v[46:49], v238 offset:3072
	ds_read_b128 v[50:53], v238 offset:4096
	ds_read_b128 v[54:57], v238 offset:5120
	ds_read_b128 v[58:61], v238 offset:6144
	ds_read_b128 v[62:65], v238 offset:7168
	global_load_lds_dwordx4 v[210:211], off
	v_lshl_add_u64 v[210:211], v[208:209], 0, s[46:47]
	s_add_i32 m0, s62, 0xe000
	s_cmp_lg_u32 s46, 0
	global_load_lds_dwordx4 v[210:211], off
	s_waitcnt vmcnt(8)
	s_waitcnt lgkmcnt(0)
	s_cselect_b64 s[56:57], -1, 0
	s_barrier
	s_setprio 1
	s_and_b64 vcc, exec, s[56:57]
	s_cbranch_vccz .LBB0_168
	s_waitcnt lgkmcnt(0)
	v_mfma_scale_f32_16x16x128_f8f6f4 v[106:109], v[2:9], v[34:41], v[106:109], v236, v237 op_sel_hi:[0,0,0]
	v_mfma_scale_f32_16x16x128_f8f6f4 v[122:125], v[18:25], v[34:41], v[122:125], v236, v237 op_sel_hi:[0,0,0]
	v_mfma_scale_f32_16x16x128_f8f6f4 v[134:137], v[2:9], v[42:49], v[134:137], v236, v237 op_sel_hi:[0,0,0]
	v_mfma_scale_f32_16x16x128_f8f6f4 v[146:149], v[18:25], v[42:49], v[146:149], v236, v237 op_sel_hi:[0,0,0]
	v_mfma_scale_f32_16x16x128_f8f6f4 v[158:161], v[2:9], v[50:57], v[158:161], v236, v237 op_sel_hi:[0,0,0]
	v_mfma_scale_f32_16x16x128_f8f6f4 v[114:117], v[18:25], v[50:57], v[114:117], v236, v237 op_sel_hi:[0,0,0]
	v_mfma_scale_f32_16x16x128_f8f6f4 v[126:129], v[2:9], v[58:65], v[126:129], v236, v237 op_sel_hi:[0,0,0]
	v_mfma_scale_f32_16x16x128_f8f6f4 v[138:141], v[18:25], v[58:65], v[138:141], v236, v237 op_sel_hi:[0,0,0]
	v_mfma_scale_f32_16x16x128_f8f6f4 v[162:165], v[10:17], v[34:41], v[162:165], v236, v237 op_sel_hi:[0,0,0]
	v_mfma_scale_f32_16x16x128_f8f6f4 v[166:169], v[26:33], v[34:41], v[166:169], v236, v237 op_sel_hi:[0,0,0]
	v_mfma_scale_f32_16x16x128_f8f6f4 v[170:173], v[10:17], v[42:49], v[170:173], v236, v237 op_sel_hi:[0,0,0]
	v_mfma_scale_f32_16x16x128_f8f6f4 v[174:177], v[26:33], v[42:49], v[174:177], v236, v237 op_sel_hi:[0,0,0]
	v_mfma_scale_f32_16x16x128_f8f6f4 v[178:181], v[10:17], v[50:57], v[178:181], v236, v237 op_sel_hi:[0,0,0]
	v_mfma_scale_f32_16x16x128_f8f6f4 v[182:185], v[26:33], v[50:57], v[182:185], v236, v237 op_sel_hi:[0,0,0]
	v_mfma_scale_f32_16x16x128_f8f6f4 v[186:189], v[10:17], v[58:65], v[186:189], v236, v237 op_sel_hi:[0,0,0]
	v_mfma_scale_f32_16x16x128_f8f6f4 v[190:193], v[26:33], v[58:65], v[190:193], v236, v237 op_sel_hi:[0,0,0]
	s_cbranch_execnz .LBB0_166
.LBB0_165:
	s_waitcnt lgkmcnt(0)
	v_mfma_scale_f32_16x16x128_f8f6f4 v[106:109], v[2:9], v[34:41], 0, v236, v237 op_sel_hi:[0,0,0]
	v_mfma_scale_f32_16x16x128_f8f6f4 v[122:125], v[18:25], v[34:41], 0, v236, v237 op_sel_hi:[0,0,0]
	v_mfma_scale_f32_16x16x128_f8f6f4 v[134:137], v[2:9], v[42:49], 0, v236, v237 op_sel_hi:[0,0,0]
	v_mfma_scale_f32_16x16x128_f8f6f4 v[146:149], v[18:25], v[42:49], 0, v236, v237 op_sel_hi:[0,0,0]
	v_mfma_scale_f32_16x16x128_f8f6f4 v[158:161], v[2:9], v[50:57], 0, v236, v237 op_sel_hi:[0,0,0]
	v_mfma_scale_f32_16x16x128_f8f6f4 v[114:117], v[18:25], v[50:57], 0, v236, v237 op_sel_hi:[0,0,0]
	v_mfma_scale_f32_16x16x128_f8f6f4 v[126:129], v[2:9], v[58:65], 0, v236, v237 op_sel_hi:[0,0,0]
	v_mfma_scale_f32_16x16x128_f8f6f4 v[138:141], v[18:25], v[58:65], 0, v236, v237 op_sel_hi:[0,0,0]
	v_mfma_scale_f32_16x16x128_f8f6f4 v[162:165], v[10:17], v[34:41], 0, v236, v237 op_sel_hi:[0,0,0]
	v_mfma_scale_f32_16x16x128_f8f6f4 v[166:169], v[26:33], v[34:41], 0, v236, v237 op_sel_hi:[0,0,0]
	v_mfma_scale_f32_16x16x128_f8f6f4 v[170:173], v[10:17], v[42:49], 0, v236, v237 op_sel_hi:[0,0,0]
	v_mfma_scale_f32_16x16x128_f8f6f4 v[174:177], v[26:33], v[42:49], 0, v236, v237 op_sel_hi:[0,0,0]
	v_mfma_scale_f32_16x16x128_f8f6f4 v[178:181], v[10:17], v[50:57], 0, v236, v237 op_sel_hi:[0,0,0]
	v_mfma_scale_f32_16x16x128_f8f6f4 v[182:185], v[26:33], v[50:57], 0, v236, v237 op_sel_hi:[0,0,0]
	v_mfma_scale_f32_16x16x128_f8f6f4 v[186:189], v[10:17], v[58:65], 0, v236, v237 op_sel_hi:[0,0,0]
	v_mfma_scale_f32_16x16x128_f8f6f4 v[190:193], v[26:33], v[58:65], 0, v236, v237 op_sel_hi:[0,0,0]
.LBB0_166:
	s_add_u32 s52, s44, s46
	s_addc_u32 s53, s45, s47
	s_add_u32 s52, s52, 0x100
	s_addc_u32 s53, s53, 0
	s_add_u32 s79, s33, s46
	s_addc_u32 s82, s43, s47
	s_cmpk_eq_i32 s46, 0x300
	s_cselect_b32 s55, s7, s53
	s_cselect_b32 s54, s8, s52
	s_cselect_b32 s53, s29, s82
	s_cselect_b32 s52, s31, s79
	s_setprio 0
	s_barrier
	s_mov_b32 m0, s63
	v_lshl_add_u64 v[216:217], s[52:53], 0, v[196:197]
	s_add_u32 s82, s52, 0x20000
	s_waitcnt lgkmcnt(0)
	ds_read_b128 v[34:37], v238 offset:16384
	ds_read_b128 v[38:41], v238 offset:17408
	ds_read_b128 v[42:45], v238 offset:18432
	ds_read_b128 v[46:49], v238 offset:19456
	ds_read_b128 v[50:53], v238 offset:20480
	ds_read_b128 v[54:57], v238 offset:21504
	ds_read_b128 v[58:61], v238 offset:22528
	ds_read_b128 v[62:65], v238 offset:23552
	global_load_lds_dwordx4 v[216:217], off
	v_lshl_add_u64 v[214:215], s[52:53], 0, v[200:201]
	s_mov_b32 m0, s64
	s_addc_u32 s83, s53, 0
	global_load_lds_dwordx4 v[214:215], off
	v_lshl_add_u64 v[210:211], s[82:83], 0, v[196:197]
	s_mov_b32 m0, s65
	v_lshl_add_u64 v[212:213], s[54:55], 0, v[198:199]
	global_load_lds_dwordx4 v[210:211], off
	v_lshl_add_u64 v[210:211], s[82:83], 0, v[200:201]
	s_mov_b32 m0, s66
	s_nop 0
	global_load_lds_dwordx4 v[210:211], off
	v_lshl_add_u64 v[210:211], s[54:55], 0, v[194:195]
	s_mov_b32 m0, s62
	s_nop 0
	global_load_lds_dwordx4 v[210:211], off
	s_mov_b32 m0, s67
	s_nop 0
	global_load_lds_dwordx4 v[212:213], off
	s_waitcnt vmcnt(8)
	s_waitcnt lgkmcnt(0)
	s_barrier
	s_setprio 1
	s_and_b64 vcc, exec, s[56:57]
	s_cbranch_vccz .LBB0_169
	s_waitcnt lgkmcnt(0)
	v_mfma_scale_f32_16x16x128_f8f6f4 v[66:69], v[2:9], v[34:41], v[66:69], v236, v237 op_sel_hi:[0,0,0]
	v_mfma_scale_f32_16x16x128_f8f6f4 v[70:73], v[18:25], v[34:41], v[70:73], v236, v237 op_sel_hi:[0,0,0]
	v_mfma_scale_f32_16x16x128_f8f6f4 v[74:77], v[2:9], v[42:49], v[74:77], v236, v237 op_sel_hi:[0,0,0]
	v_mfma_scale_f32_16x16x128_f8f6f4 v[78:81], v[18:25], v[42:49], v[78:81], v236, v237 op_sel_hi:[0,0,0]
	v_mfma_scale_f32_16x16x128_f8f6f4 v[82:85], v[2:9], v[50:57], v[82:85], v236, v237 op_sel_hi:[0,0,0]
	v_mfma_scale_f32_16x16x128_f8f6f4 v[86:89], v[18:25], v[50:57], v[86:89], v236, v237 op_sel_hi:[0,0,0]
	v_mfma_scale_f32_16x16x128_f8f6f4 v[90:93], v[2:9], v[58:65], v[90:93], v236, v237 op_sel_hi:[0,0,0]
	v_mfma_scale_f32_16x16x128_f8f6f4 v[94:97], v[18:25], v[58:65], v[94:97], v236, v237 op_sel_hi:[0,0,0]
	v_mfma_scale_f32_16x16x128_f8f6f4 v[98:101], v[10:17], v[34:41], v[98:101], v236, v237 op_sel_hi:[0,0,0]
	v_mfma_scale_f32_16x16x128_f8f6f4 v[102:105], v[26:33], v[34:41], v[102:105], v236, v237 op_sel_hi:[0,0,0]
	v_mfma_scale_f32_16x16x128_f8f6f4 v[110:113], v[10:17], v[42:49], v[110:113], v236, v237 op_sel_hi:[0,0,0]
	v_mfma_scale_f32_16x16x128_f8f6f4 v[118:121], v[26:33], v[42:49], v[118:121], v236, v237 op_sel_hi:[0,0,0]
	v_mfma_scale_f32_16x16x128_f8f6f4 v[130:133], v[10:17], v[50:57], v[130:133], v236, v237 op_sel_hi:[0,0,0]
	v_mfma_scale_f32_16x16x128_f8f6f4 v[142:145], v[26:33], v[50:57], v[142:145], v236, v237 op_sel_hi:[0,0,0]
	v_mfma_scale_f32_16x16x128_f8f6f4 v[150:153], v[10:17], v[58:65], v[150:153], v236, v237 op_sel_hi:[0,0,0]
	v_mfma_scale_f32_16x16x128_f8f6f4 v[154:157], v[26:33], v[58:65], v[154:157], v236, v237 op_sel_hi:[0,0,0]
	s_cbranch_execnz .LBB0_162
	s_branch .LBB0_170

.LBB0_169:
.LBB0_170:
	s_waitcnt lgkmcnt(0)
	v_mfma_scale_f32_16x16x128_f8f6f4 v[66:69], v[2:9], v[34:41], 0, v236, v237 op_sel_hi:[0,0,0]
	v_mfma_scale_f32_16x16x128_f8f6f4 v[70:73], v[18:25], v[34:41], 0, v236, v237 op_sel_hi:[0,0,0]
	v_mfma_scale_f32_16x16x128_f8f6f4 v[74:77], v[2:9], v[42:49], 0, v236, v237 op_sel_hi:[0,0,0]
	v_mfma_scale_f32_16x16x128_f8f6f4 v[78:81], v[18:25], v[42:49], 0, v236, v237 op_sel_hi:[0,0,0]
	v_mfma_scale_f32_16x16x128_f8f6f4 v[82:85], v[2:9], v[50:57], 0, v236, v237 op_sel_hi:[0,0,0]
	v_mfma_scale_f32_16x16x128_f8f6f4 v[86:89], v[18:25], v[50:57], 0, v236, v237 op_sel_hi:[0,0,0]
	v_mfma_scale_f32_16x16x128_f8f6f4 v[90:93], v[2:9], v[58:65], 0, v236, v237 op_sel_hi:[0,0,0]
	v_mfma_scale_f32_16x16x128_f8f6f4 v[94:97], v[18:25], v[58:65], 0, v236, v237 op_sel_hi:[0,0,0]
	v_mfma_scale_f32_16x16x128_f8f6f4 v[98:101], v[10:17], v[34:41], 0, v236, v237 op_sel_hi:[0,0,0]
	v_mfma_scale_f32_16x16x128_f8f6f4 v[102:105], v[26:33], v[34:41], 0, v236, v237 op_sel_hi:[0,0,0]
	v_mfma_scale_f32_16x16x128_f8f6f4 v[110:113], v[10:17], v[42:49], 0, v236, v237 op_sel_hi:[0,0,0]
	v_mfma_scale_f32_16x16x128_f8f6f4 v[118:121], v[26:33], v[42:49], 0, v236, v237 op_sel_hi:[0,0,0]
	v_mfma_scale_f32_16x16x128_f8f6f4 v[130:133], v[10:17], v[50:57], 0, v236, v237 op_sel_hi:[0,0,0]
	v_mfma_scale_f32_16x16x128_f8f6f4 v[142:145], v[26:33], v[50:57], 0, v236, v237 op_sel_hi:[0,0,0]
	v_mfma_scale_f32_16x16x128_f8f6f4 v[150:153], v[10:17], v[58:65], 0, v236, v237 op_sel_hi:[0,0,0]
	v_mfma_scale_f32_16x16x128_f8f6f4 v[154:157], v[26:33], v[58:65], 0, v236, v237 op_sel_hi:[0,0,0]
	s_branch .LBB0_162

.LBB0_759:
	s_setprio 0
	s_barrier
	s_add_i32 s34, 0, 0x18000
	s_add_i32 s35, 0, 0x1c000
	v_add_u32_e32 v142, s34, v203
	v_add_u32_e32 v158, s35, v203
	ds_read_b128 v[130:133], v142
	ds_read_b128 v[134:137], v142 offset:1024
	ds_read_b128 v[138:141], v142 offset:2048
	ds_read_b128 v[142:145], v142 offset:3072
	ds_read_b128 v[146:149], v158
	ds_read_b128 v[150:153], v158 offset:1024
	ds_read_b128 v[154:157], v158 offset:2048
	ds_read_b128 v[158:161], v158 offset:3072
	s_add_u32 s30, s30, 0x40000
	s_addc_u32 s31, s31, 0
	s_mov_b32 m0, s49
	v_lshl_add_u64 v[224:225], s[30:31], 0, v[200:201]
	s_waitcnt lgkmcnt(0)
	ds_read_b128 v[162:165], v222 offset:32768
	ds_read_b128 v[166:169], v222 offset:33792
	ds_read_b128 v[170:173], v222 offset:34816
	ds_read_b128 v[174:177], v222 offset:35840
	ds_read_b128 v[178:181], v222 offset:36864
	ds_read_b128 v[182:185], v222 offset:37888
	ds_read_b128 v[186:189], v222 offset:38912
	ds_read_b128 v[190:193], v222 offset:39936
	global_load_lds_dwordx4 v[224:225], off
	v_lshl_add_u64 v[224:225], s[30:31], 0, v[196:197]
	s_mov_b32 m0, s50
	s_nop 0
	global_load_lds_dwordx4 v[224:225], off
	s_waitcnt vmcnt(8)
	s_waitcnt lgkmcnt(0)
	s_barrier
	s_setprio 1
	s_waitcnt lgkmcnt(0)
	v_mfma_f32_16x16x32_bf16 v[126:129], v[130:133], v[162:165], v[126:129]
	v_mfma_f32_16x16x32_bf16 v[122:125], v[138:141], v[162:165], v[122:125]
	v_mfma_f32_16x16x32_bf16 v[118:121], v[130:133], v[170:173], v[118:121]
	v_mfma_f32_16x16x32_bf16 v[114:117], v[138:141], v[170:173], v[114:117]
	v_mfma_f32_16x16x32_bf16 v[110:113], v[130:133], v[178:181], v[110:113]
	v_mfma_f32_16x16x32_bf16 v[106:109], v[138:141], v[178:181], v[106:109]
	v_mfma_f32_16x16x32_bf16 v[102:105], v[130:133], v[186:189], v[102:105]
	v_mfma_f32_16x16x32_bf16 v[98:101], v[138:141], v[186:189], v[98:101]
	v_mfma_f32_16x16x32_bf16 v[126:129], v[134:137], v[166:169], v[126:129]
	v_mfma_f32_16x16x32_bf16 v[122:125], v[142:145], v[166:169], v[122:125]
	v_mfma_f32_16x16x32_bf16 v[118:121], v[134:137], v[174:177], v[118:121]
	v_mfma_f32_16x16x32_bf16 v[114:117], v[142:145], v[174:177], v[114:117]
	v_mfma_f32_16x16x32_bf16 v[110:113], v[134:137], v[182:185], v[110:113]
	v_mfma_f32_16x16x32_bf16 v[106:109], v[142:145], v[182:185], v[106:109]
	v_mfma_f32_16x16x32_bf16 v[102:105], v[134:137], v[190:193], v[102:105]
	v_mfma_f32_16x16x32_bf16 v[98:101], v[142:145], v[190:193], v[98:101]
	v_mfma_f32_16x16x32_bf16 v[94:97], v[146:149], v[162:165], v[94:97]
	v_mfma_f32_16x16x32_bf16 v[90:93], v[154:157], v[162:165], v[90:93]
	v_mfma_f32_16x16x32_bf16 v[86:89], v[146:149], v[170:173], v[86:89]
	v_mfma_f32_16x16x32_bf16 v[82:85], v[154:157], v[170:173], v[82:85]
	v_mfma_f32_16x16x32_bf16 v[78:81], v[146:149], v[178:181], v[78:81]
	v_mfma_f32_16x16x32_bf16 v[74:77], v[154:157], v[178:181], v[74:77]
	v_mfma_f32_16x16x32_bf16 v[70:73], v[146:149], v[186:189], v[70:73]
	v_mfma_f32_16x16x32_bf16 v[66:69], v[154:157], v[186:189], v[66:69]
	v_mfma_f32_16x16x32_bf16 v[94:97], v[150:153], v[166:169], v[94:97]
	v_mfma_f32_16x16x32_bf16 v[90:93], v[158:161], v[166:169], v[90:93]
	v_mfma_f32_16x16x32_bf16 v[86:89], v[150:153], v[174:177], v[86:89]
	v_mfma_f32_16x16x32_bf16 v[82:85], v[158:161], v[174:177], v[82:85]
	v_mfma_f32_16x16x32_bf16 v[78:81], v[150:153], v[182:185], v[78:81]
	v_mfma_f32_16x16x32_bf16 v[74:77], v[158:161], v[182:185], v[74:77]
	v_mfma_f32_16x16x32_bf16 v[70:73], v[150:153], v[190:193], v[70:73]
	v_mfma_f32_16x16x32_bf16 v[66:69], v[158:161], v[190:193], v[66:69]
	s_setprio 0
	s_barrier
	s_add_i32 s30, s34, s42
	v_lshl_add_u64 v[220:221], v[220:221], 0, s[8:9]
	s_mov_b32 m0, s30
	ds_read_b128 v[162:165], v222 offset:49152
	ds_read_b128 v[166:169], v222 offset:50176
	ds_read_b128 v[170:173], v222 offset:51200
	ds_read_b128 v[174:177], v222 offset:52224
	ds_read_b128 v[178:181], v222 offset:53248
	ds_read_b128 v[182:185], v222 offset:54272
	ds_read_b128 v[186:189], v222 offset:55296
	ds_read_b128 v[190:193], v222 offset:56320
	global_load_lds_dwordx4 v[220:221], off
	s_add_i32 m0, s30, 0x2000
	s_add_u32 s28, s28, 0x40080
	v_lshl_add_u64 v[218:219], v[218:219], 0, s[8:9]
	s_addc_u32 s29, s29, 0
	s_add_i32 s30, s35, s42
	global_load_lds_dwordx4 v[218:219], off
	v_lshl_add_u64 v[218:219], s[28:29], 0, v[198:199]
	s_mov_b32 m0, s30
	v_lshl_add_u64 v[214:215], v[214:215], 0, s[8:9]
	global_load_lds_dwordx4 v[218:219], off
	v_lshl_add_u64 v[218:219], s[28:29], 0, v[194:195]
	s_add_i32 m0, s30, 0x2000
	s_nop 0
	global_load_lds_dwordx4 v[218:219], off
	s_mov_b32 m0, s53
	s_nop 0
	global_load_lds_dwordx4 v[214:215], off
	v_lshl_add_u64 v[214:215], v[216:217], 0, s[8:9]
	s_mov_b32 m0, s54
	s_nop 0
	global_load_lds_dwordx4 v[214:215], off
	s_waitcnt vmcnt(8)
	s_waitcnt lgkmcnt(0)
	s_barrier
	s_setprio 1
	s_waitcnt lgkmcnt(0)
	v_mfma_f32_16x16x32_bf16 v[62:65], v[130:133], v[162:165], v[62:65]
	v_mfma_f32_16x16x32_bf16 v[58:61], v[138:141], v[162:165], v[58:61]
	v_mfma_f32_16x16x32_bf16 v[54:57], v[130:133], v[170:173], v[54:57]
	v_mfma_f32_16x16x32_bf16 v[50:53], v[138:141], v[170:173], v[50:53]
	v_mfma_f32_16x16x32_bf16 v[46:49], v[130:133], v[178:181], v[46:49]
	v_mfma_f32_16x16x32_bf16 v[42:45], v[138:141], v[178:181], v[42:45]
	v_mfma_f32_16x16x32_bf16 v[38:41], v[130:133], v[186:189], v[38:41]
	v_mfma_f32_16x16x32_bf16 v[34:37], v[138:141], v[186:189], v[34:37]
	v_mfma_f32_16x16x32_bf16 v[62:65], v[134:137], v[166:169], v[62:65]
	v_mfma_f32_16x16x32_bf16 v[58:61], v[142:145], v[166:169], v[58:61]
	v_mfma_f32_16x16x32_bf16 v[54:57], v[134:137], v[174:177], v[54:57]
	v_mfma_f32_16x16x32_bf16 v[50:53], v[142:145], v[174:177], v[50:53]
	v_mfma_f32_16x16x32_bf16 v[46:49], v[134:137], v[182:185], v[46:49]
	v_mfma_f32_16x16x32_bf16 v[42:45], v[142:145], v[182:185], v[42:45]
	v_mfma_f32_16x16x32_bf16 v[38:41], v[134:137], v[190:193], v[38:41]
	v_mfma_f32_16x16x32_bf16 v[34:37], v[142:145], v[190:193], v[34:37]
	v_mfma_f32_16x16x32_bf16 v[30:33], v[146:149], v[162:165], v[30:33]
	v_mfma_f32_16x16x32_bf16 v[26:29], v[154:157], v[162:165], v[26:29]
	v_mfma_f32_16x16x32_bf16 v[22:25], v[146:149], v[170:173], v[22:25]
	v_mfma_f32_16x16x32_bf16 v[18:21], v[154:157], v[170:173], v[18:21]
	v_mfma_f32_16x16x32_bf16 v[14:17], v[146:149], v[178:181], v[14:17]
	v_mfma_f32_16x16x32_bf16 v[10:13], v[154:157], v[178:181], v[10:13]
	v_mfma_f32_16x16x32_bf16 v[6:9], v[146:149], v[186:189], v[6:9]
	v_mfma_f32_16x16x32_bf16 v[2:5], v[154:157], v[186:189], v[2:5]
	v_mfma_f32_16x16x32_bf16 v[30:33], v[150:153], v[166:169], v[30:33]
	v_mfma_f32_16x16x32_bf16 v[26:29], v[158:161], v[166:169], v[26:29]
	v_mfma_f32_16x16x32_bf16 v[22:25], v[150:153], v[174:177], v[22:25]
	v_mfma_f32_16x16x32_bf16 v[18:21], v[158:161], v[174:177], v[18:21]
	v_mfma_f32_16x16x32_bf16 v[14:17], v[150:153], v[182:185], v[14:17]
	v_mfma_f32_16x16x32_bf16 v[10:13], v[158:161], v[182:185], v[10:13]
	v_mfma_f32_16x16x32_bf16 v[6:9], v[150:153], v[190:193], v[6:9]
	v_mfma_f32_16x16x32_bf16 v[2:5], v[158:161], v[190:193], v[2:5]
	s_setprio 0
	s_barrier
	s_add_i32 s72, s72, 2
	s_add_u32 s26, s26, 0x100
	s_addc_u32 s27, s27, 0
	s_cmp_gt_u32 s72, 13
	s_cbranch_scc1 .LBB0_770

.LBB0_762:
	v_add_u32_e32 v130, 0, v203
	v_add_u32_e32 v131, 0x10000, v130
	v_add_u32_e32 v142, 0x14000, v130
	ds_read_b128 v[146:149], v131
	ds_read_b128 v[150:153], v131 offset:1024
	ds_read_b128 v[154:157], v131 offset:2048
	ds_read_b128 v[158:161], v131 offset:3072
	ds_read_b128 v[130:133], v142
	ds_read_b128 v[134:137], v142 offset:1024
	ds_read_b128 v[138:141], v142 offset:2048
	ds_read_b128 v[142:145], v142 offset:3072
	v_lshl_add_u64 v[214:215], v[210:211], 0, s[26:27]
	s_add_i32 m0, s43, 0xc000
	ds_read_b128 v[186:189], v222
	ds_read_b128 v[190:193], v222 offset:1024
	ds_read_b128 v[178:181], v222 offset:2048
	ds_read_b128 v[182:185], v222 offset:3072
	ds_read_b128 v[170:173], v222 offset:4096
	ds_read_b128 v[174:177], v222 offset:5120
	ds_read_b128 v[162:165], v222 offset:6144
	ds_read_b128 v[166:169], v222 offset:7168
	global_load_lds_dwordx4 v[214:215], off
	v_lshl_add_u64 v[214:215], v[212:213], 0, s[26:27]
	s_add_i32 m0, s43, 0xe000
	s_cmp_lg_u32 s26, 0
	global_load_lds_dwordx4 v[214:215], off
	s_waitcnt vmcnt(8)
	s_waitcnt lgkmcnt(0)
	s_cselect_b64 s[34:35], -1, 0
	s_barrier
	s_setprio 1
	s_and_b64 vcc, exec, s[34:35]
	s_cbranch_vccz .LBB0_767
	s_waitcnt lgkmcnt(0)
	v_mfma_f32_16x16x32_bf16 v[126:129], v[146:149], v[186:189], v[126:129]
	v_mfma_f32_16x16x32_bf16 v[122:125], v[154:157], v[186:189], v[122:125]
	v_mfma_f32_16x16x32_bf16 v[118:121], v[146:149], v[178:181], v[118:121]
	v_mfma_f32_16x16x32_bf16 v[114:117], v[154:157], v[178:181], v[114:117]
	v_mfma_f32_16x16x32_bf16 v[110:113], v[146:149], v[170:173], v[110:113]
	v_mfma_f32_16x16x32_bf16 v[106:109], v[154:157], v[170:173], v[106:109]
	v_mfma_f32_16x16x32_bf16 v[102:105], v[146:149], v[162:165], v[102:105]
	v_mfma_f32_16x16x32_bf16 v[98:101], v[154:157], v[162:165], v[98:101]
	v_mfma_f32_16x16x32_bf16 v[126:129], v[150:153], v[190:193], v[126:129]
	v_mfma_f32_16x16x32_bf16 v[122:125], v[158:161], v[190:193], v[122:125]
	v_mfma_f32_16x16x32_bf16 v[118:121], v[150:153], v[182:185], v[118:121]
	v_mfma_f32_16x16x32_bf16 v[114:117], v[158:161], v[182:185], v[114:117]
	v_mfma_f32_16x16x32_bf16 v[110:113], v[150:153], v[174:177], v[110:113]
	v_mfma_f32_16x16x32_bf16 v[106:109], v[158:161], v[174:177], v[106:109]
	v_mfma_f32_16x16x32_bf16 v[102:105], v[150:153], v[166:169], v[102:105]
	v_mfma_f32_16x16x32_bf16 v[98:101], v[158:161], v[166:169], v[98:101]
	v_mfma_f32_16x16x32_bf16 v[94:97], v[130:133], v[186:189], v[94:97]
	v_mfma_f32_16x16x32_bf16 v[90:93], v[138:141], v[186:189], v[90:93]
	v_mfma_f32_16x16x32_bf16 v[86:89], v[130:133], v[178:181], v[86:89]
	v_mfma_f32_16x16x32_bf16 v[82:85], v[138:141], v[178:181], v[82:85]
	v_mfma_f32_16x16x32_bf16 v[78:81], v[130:133], v[170:173], v[78:81]
	v_mfma_f32_16x16x32_bf16 v[74:77], v[138:141], v[170:173], v[74:77]
	v_mfma_f32_16x16x32_bf16 v[70:73], v[130:133], v[162:165], v[70:73]
	v_mfma_f32_16x16x32_bf16 v[66:69], v[138:141], v[162:165], v[66:69]
	v_mfma_f32_16x16x32_bf16 v[94:97], v[134:137], v[190:193], v[94:97]
	v_mfma_f32_16x16x32_bf16 v[90:93], v[142:145], v[190:193], v[90:93]
	v_mfma_f32_16x16x32_bf16 v[86:89], v[134:137], v[182:185], v[86:89]
	v_mfma_f32_16x16x32_bf16 v[82:85], v[142:145], v[182:185], v[82:85]
	v_mfma_f32_16x16x32_bf16 v[78:81], v[134:137], v[174:177], v[78:81]
	v_mfma_f32_16x16x32_bf16 v[74:77], v[142:145], v[174:177], v[74:77]
	v_mfma_f32_16x16x32_bf16 v[70:73], v[134:137], v[166:169], v[70:73]
	v_mfma_f32_16x16x32_bf16 v[66:69], v[142:145], v[166:169], v[66:69]
	s_cbranch_execnz .LBB0_765
.LBB0_764:
	s_waitcnt lgkmcnt(0)
	v_mfma_f32_16x16x32_bf16 v[66:69], v[146:149], v[186:189], 0
	v_mfma_f32_16x16x32_bf16 v[126:129], v[150:153], v[190:193], v[66:69]
	v_mfma_f32_16x16x32_bf16 v[66:69], v[154:157], v[186:189], 0
	v_mfma_f32_16x16x32_bf16 v[122:125], v[158:161], v[190:193], v[66:69]
	v_mfma_f32_16x16x32_bf16 v[66:69], v[146:149], v[178:181], 0
	v_mfma_f32_16x16x32_bf16 v[118:121], v[150:153], v[182:185], v[66:69]
	v_mfma_f32_16x16x32_bf16 v[66:69], v[154:157], v[178:181], 0
	v_mfma_f32_16x16x32_bf16 v[114:117], v[158:161], v[182:185], v[66:69]
	v_mfma_f32_16x16x32_bf16 v[66:69], v[146:149], v[170:173], 0
	v_mfma_f32_16x16x32_bf16 v[110:113], v[150:153], v[174:177], v[66:69]
	v_mfma_f32_16x16x32_bf16 v[66:69], v[154:157], v[170:173], 0
	v_mfma_f32_16x16x32_bf16 v[106:109], v[158:161], v[174:177], v[66:69]
	v_mfma_f32_16x16x32_bf16 v[66:69], v[146:149], v[162:165], 0
	v_mfma_f32_16x16x32_bf16 v[102:105], v[150:153], v[166:169], v[66:69]
	v_mfma_f32_16x16x32_bf16 v[66:69], v[154:157], v[162:165], 0
	v_mfma_f32_16x16x32_bf16 v[98:101], v[158:161], v[166:169], v[66:69]
	v_mfma_f32_16x16x32_bf16 v[66:69], v[130:133], v[186:189], 0
	v_mfma_f32_16x16x32_bf16 v[94:97], v[134:137], v[190:193], v[66:69]
	v_mfma_f32_16x16x32_bf16 v[66:69], v[138:141], v[186:189], 0
	v_mfma_f32_16x16x32_bf16 v[90:93], v[142:145], v[190:193], v[66:69]
	v_mfma_f32_16x16x32_bf16 v[66:69], v[130:133], v[178:181], 0
	v_mfma_f32_16x16x32_bf16 v[86:89], v[134:137], v[182:185], v[66:69]
	v_mfma_f32_16x16x32_bf16 v[66:69], v[138:141], v[178:181], 0
	v_mfma_f32_16x16x32_bf16 v[82:85], v[142:145], v[182:185], v[66:69]
	v_mfma_f32_16x16x32_bf16 v[66:69], v[130:133], v[170:173], 0
	v_mfma_f32_16x16x32_bf16 v[78:81], v[134:137], v[174:177], v[66:69]
	v_mfma_f32_16x16x32_bf16 v[66:69], v[138:141], v[170:173], 0
	v_mfma_f32_16x16x32_bf16 v[74:77], v[142:145], v[174:177], v[66:69]
	v_mfma_f32_16x16x32_bf16 v[66:69], v[130:133], v[162:165], 0
	v_mfma_f32_16x16x32_bf16 v[70:73], v[134:137], v[166:169], v[66:69]
	v_mfma_f32_16x16x32_bf16 v[66:69], v[138:141], v[162:165], 0
	v_mfma_f32_16x16x32_bf16 v[66:69], v[142:145], v[166:169], v[66:69]
.LBB0_765:
	s_add_u32 s28, s22, s26
	s_addc_u32 s29, s23, s27
	s_add_u32 s28, s28, 0x100
	s_addc_u32 s29, s29, 0
	s_add_u32 s73, s70, s26
	s_addc_u32 s74, s71, s27
	s_cmpk_eq_i32 s26, 0x700
	s_cselect_b32 s31, s15, s29
	s_cselect_b32 s30, s33, s28
	s_cselect_b32 s29, s61, s74
	s_cselect_b32 s28, s62, s73
	s_setprio 0
	s_barrier
	s_mov_b32 m0, s44
	v_lshl_add_u64 v[220:221], s[28:29], 0, v[198:199]
	s_add_u32 s74, s28, 0x40000
	s_waitcnt lgkmcnt(0)
	ds_read_b128 v[186:189], v222 offset:16384
	ds_read_b128 v[190:193], v222 offset:17408
	ds_read_b128 v[178:181], v222 offset:18432
	ds_read_b128 v[182:185], v222 offset:19456
	ds_read_b128 v[170:173], v222 offset:20480
	ds_read_b128 v[174:177], v222 offset:21504
	ds_read_b128 v[162:165], v222 offset:22528
	ds_read_b128 v[166:169], v222 offset:23552
	global_load_lds_dwordx4 v[220:221], off
	v_lshl_add_u64 v[218:219], s[28:29], 0, v[194:195]
	s_mov_b32 m0, s45
	s_addc_u32 s75, s29, 0
	global_load_lds_dwordx4 v[218:219], off
	v_lshl_add_u64 v[214:215], s[74:75], 0, v[198:199]
	s_mov_b32 m0, s46
	v_lshl_add_u64 v[216:217], s[30:31], 0, v[196:197]
	global_load_lds_dwordx4 v[214:215], off
	v_lshl_add_u64 v[214:215], s[74:75], 0, v[194:195]
	s_mov_b32 m0, s47
	s_nop 0
	global_load_lds_dwordx4 v[214:215], off
	v_lshl_add_u64 v[214:215], s[30:31], 0, v[200:201]
	s_mov_b32 m0, s43
	s_nop 0
	global_load_lds_dwordx4 v[214:215], off
	s_mov_b32 m0, s48
	s_nop 0
	global_load_lds_dwordx4 v[216:217], off
	s_waitcnt vmcnt(8)
	s_waitcnt lgkmcnt(0)
	s_barrier
	s_setprio 1
	s_and_b64 vcc, exec, s[34:35]
	s_cbranch_vccz .LBB0_768
	s_waitcnt lgkmcnt(0)
	v_mfma_f32_16x16x32_bf16 v[62:65], v[146:149], v[186:189], v[62:65]
	v_mfma_f32_16x16x32_bf16 v[58:61], v[154:157], v[186:189], v[58:61]
	v_mfma_f32_16x16x32_bf16 v[54:57], v[146:149], v[178:181], v[54:57]
	v_mfma_f32_16x16x32_bf16 v[50:53], v[154:157], v[178:181], v[50:53]
	v_mfma_f32_16x16x32_bf16 v[46:49], v[146:149], v[170:173], v[46:49]
	v_mfma_f32_16x16x32_bf16 v[42:45], v[154:157], v[170:173], v[42:45]
	v_mfma_f32_16x16x32_bf16 v[38:41], v[146:149], v[162:165], v[38:41]
	v_mfma_f32_16x16x32_bf16 v[34:37], v[154:157], v[162:165], v[34:37]
	v_mfma_f32_16x16x32_bf16 v[62:65], v[150:153], v[190:193], v[62:65]
	v_mfma_f32_16x16x32_bf16 v[58:61], v[158:161], v[190:193], v[58:61]
	v_mfma_f32_16x16x32_bf16 v[54:57], v[150:153], v[182:185], v[54:57]
	v_mfma_f32_16x16x32_bf16 v[50:53], v[158:161], v[182:185], v[50:53]
	v_mfma_f32_16x16x32_bf16 v[46:49], v[150:153], v[174:177], v[46:49]
	v_mfma_f32_16x16x32_bf16 v[42:45], v[158:161], v[174:177], v[42:45]
	v_mfma_f32_16x16x32_bf16 v[38:41], v[150:153], v[166:169], v[38:41]
	v_mfma_f32_16x16x32_bf16 v[34:37], v[158:161], v[166:169], v[34:37]
	v_mfma_f32_16x16x32_bf16 v[30:33], v[130:133], v[186:189], v[30:33]
	v_mfma_f32_16x16x32_bf16 v[26:29], v[138:141], v[186:189], v[26:29]
	v_mfma_f32_16x16x32_bf16 v[22:25], v[130:133], v[178:181], v[22:25]
	v_mfma_f32_16x16x32_bf16 v[18:21], v[138:141], v[178:181], v[18:21]
	v_mfma_f32_16x16x32_bf16 v[14:17], v[130:133], v[170:173], v[14:17]
	v_mfma_f32_16x16x32_bf16 v[10:13], v[138:141], v[170:173], v[10:13]
	v_mfma_f32_16x16x32_bf16 v[6:9], v[130:133], v[162:165], v[6:9]
	v_mfma_f32_16x16x32_bf16 v[2:5], v[138:141], v[162:165], v[2:5]
	v_mfma_f32_16x16x32_bf16 v[30:33], v[134:137], v[190:193], v[30:33]
	v_mfma_f32_16x16x32_bf16 v[26:29], v[142:145], v[190:193], v[26:29]
	v_mfma_f32_16x16x32_bf16 v[22:25], v[134:137], v[182:185], v[22:25]
	v_mfma_f32_16x16x32_bf16 v[18:21], v[142:145], v[182:185], v[18:21]
	v_mfma_f32_16x16x32_bf16 v[14:17], v[134:137], v[174:177], v[14:17]
	v_mfma_f32_16x16x32_bf16 v[10:13], v[142:145], v[174:177], v[10:13]
	v_mfma_f32_16x16x32_bf16 v[6:9], v[134:137], v[166:169], v[6:9]
	v_mfma_f32_16x16x32_bf16 v[2:5], v[142:145], v[166:169], v[2:5]
	s_cbranch_execnz .LBB0_759
	s_branch .LBB0_769

.LBB0_768:
.LBB0_769:
	s_waitcnt lgkmcnt(0)
	v_mfma_f32_16x16x32_bf16 v[2:5], v[146:149], v[186:189], 0
	v_mfma_f32_16x16x32_bf16 v[62:65], v[150:153], v[190:193], v[2:5]
	v_mfma_f32_16x16x32_bf16 v[2:5], v[154:157], v[186:189], 0
	v_mfma_f32_16x16x32_bf16 v[58:61], v[158:161], v[190:193], v[2:5]
	v_mfma_f32_16x16x32_bf16 v[2:5], v[146:149], v[178:181], 0
	v_mfma_f32_16x16x32_bf16 v[54:57], v[150:153], v[182:185], v[2:5]
	v_mfma_f32_16x16x32_bf16 v[2:5], v[154:157], v[178:181], 0
	v_mfma_f32_16x16x32_bf16 v[50:53], v[158:161], v[182:185], v[2:5]
	v_mfma_f32_16x16x32_bf16 v[2:5], v[146:149], v[170:173], 0
	v_mfma_f32_16x16x32_bf16 v[46:49], v[150:153], v[174:177], v[2:5]
	v_mfma_f32_16x16x32_bf16 v[2:5], v[154:157], v[170:173], 0
	v_mfma_f32_16x16x32_bf16 v[42:45], v[158:161], v[174:177], v[2:5]
	v_mfma_f32_16x16x32_bf16 v[2:5], v[146:149], v[162:165], 0
	v_mfma_f32_16x16x32_bf16 v[38:41], v[150:153], v[166:169], v[2:5]
	v_mfma_f32_16x16x32_bf16 v[2:5], v[154:157], v[162:165], 0
	v_mfma_f32_16x16x32_bf16 v[34:37], v[158:161], v[166:169], v[2:5]
	v_mfma_f32_16x16x32_bf16 v[2:5], v[130:133], v[186:189], 0
	v_mfma_f32_16x16x32_bf16 v[30:33], v[134:137], v[190:193], v[2:5]
	v_mfma_f32_16x16x32_bf16 v[2:5], v[138:141], v[186:189], 0
	v_mfma_f32_16x16x32_bf16 v[26:29], v[142:145], v[190:193], v[2:5]
	v_mfma_f32_16x16x32_bf16 v[2:5], v[130:133], v[178:181], 0
	v_mfma_f32_16x16x32_bf16 v[22:25], v[134:137], v[182:185], v[2:5]
	v_mfma_f32_16x16x32_bf16 v[2:5], v[138:141], v[178:181], 0
	v_mfma_f32_16x16x32_bf16 v[18:21], v[142:145], v[182:185], v[2:5]
	v_mfma_f32_16x16x32_bf16 v[2:5], v[130:133], v[170:173], 0
	v_mfma_f32_16x16x32_bf16 v[14:17], v[134:137], v[174:177], v[2:5]
	v_mfma_f32_16x16x32_bf16 v[2:5], v[138:141], v[170:173], 0
	v_mfma_f32_16x16x32_bf16 v[10:13], v[142:145], v[174:177], v[2:5]
	v_mfma_f32_16x16x32_bf16 v[2:5], v[130:133], v[162:165], 0
	v_mfma_f32_16x16x32_bf16 v[6:9], v[134:137], v[166:169], v[2:5]
	v_mfma_f32_16x16x32_bf16 v[2:5], v[138:141], v[162:165], 0
	v_mfma_f32_16x16x32_bf16 v[2:5], v[142:145], v[166:169], v[2:5]
	s_branch .LBB0_759

.LBB0_836:
	s_setprio 0
	s_barrier
	s_add_i32 s48, 0, 0x18000
	s_add_i32 s49, 0, 0x1c000
	v_add_u32_e32 v142, s48, v203
	v_add_u32_e32 v158, s49, v203
	ds_read_b128 v[130:133], v142
	ds_read_b128 v[134:137], v142 offset:1024
	ds_read_b128 v[138:141], v142 offset:2048
	ds_read_b128 v[142:145], v142 offset:3072
	ds_read_b128 v[146:149], v158
	ds_read_b128 v[150:153], v158 offset:1024
	ds_read_b128 v[154:157], v158 offset:2048
	ds_read_b128 v[158:161], v158 offset:3072
	s_add_u32 s46, s46, 0x40000
	s_addc_u32 s47, s47, 0
	s_mov_b32 m0, s58
	v_lshl_add_u64 v[222:223], s[46:47], 0, v[200:201]
	s_waitcnt lgkmcnt(0)
	ds_read_b128 v[162:165], v220 offset:32768
	ds_read_b128 v[166:169], v220 offset:33792
	ds_read_b128 v[170:173], v220 offset:34816
	ds_read_b128 v[174:177], v220 offset:35840
	ds_read_b128 v[178:181], v220 offset:36864
	ds_read_b128 v[182:185], v220 offset:37888
	ds_read_b128 v[186:189], v220 offset:38912
	ds_read_b128 v[190:193], v220 offset:39936
	global_load_lds_dwordx4 v[222:223], off
	v_lshl_add_u64 v[222:223], s[46:47], 0, v[196:197]
	s_mov_b32 m0, s59
	s_nop 0
	global_load_lds_dwordx4 v[222:223], off
	s_waitcnt vmcnt(8)
	s_waitcnt lgkmcnt(0)
	s_barrier
	s_setprio 1
	s_waitcnt lgkmcnt(0)
	v_mfma_f32_16x16x32_bf16 v[126:129], v[130:133], v[162:165], v[126:129]
	v_mfma_f32_16x16x32_bf16 v[122:125], v[138:141], v[162:165], v[122:125]
	v_mfma_f32_16x16x32_bf16 v[118:121], v[130:133], v[170:173], v[118:121]
	v_mfma_f32_16x16x32_bf16 v[114:117], v[138:141], v[170:173], v[114:117]
	v_mfma_f32_16x16x32_bf16 v[110:113], v[130:133], v[178:181], v[110:113]
	v_mfma_f32_16x16x32_bf16 v[106:109], v[138:141], v[178:181], v[106:109]
	v_mfma_f32_16x16x32_bf16 v[102:105], v[130:133], v[186:189], v[102:105]
	v_mfma_f32_16x16x32_bf16 v[98:101], v[138:141], v[186:189], v[98:101]
	v_mfma_f32_16x16x32_bf16 v[126:129], v[134:137], v[166:169], v[126:129]
	v_mfma_f32_16x16x32_bf16 v[122:125], v[142:145], v[166:169], v[122:125]
	v_mfma_f32_16x16x32_bf16 v[118:121], v[134:137], v[174:177], v[118:121]
	v_mfma_f32_16x16x32_bf16 v[114:117], v[142:145], v[174:177], v[114:117]
	v_mfma_f32_16x16x32_bf16 v[110:113], v[134:137], v[182:185], v[110:113]
	v_mfma_f32_16x16x32_bf16 v[106:109], v[142:145], v[182:185], v[106:109]
	v_mfma_f32_16x16x32_bf16 v[102:105], v[134:137], v[190:193], v[102:105]
	v_mfma_f32_16x16x32_bf16 v[98:101], v[142:145], v[190:193], v[98:101]
	v_mfma_f32_16x16x32_bf16 v[94:97], v[146:149], v[162:165], v[94:97]
	v_mfma_f32_16x16x32_bf16 v[90:93], v[154:157], v[162:165], v[90:93]
	v_mfma_f32_16x16x32_bf16 v[86:89], v[146:149], v[170:173], v[86:89]
	v_mfma_f32_16x16x32_bf16 v[82:85], v[154:157], v[170:173], v[82:85]
	v_mfma_f32_16x16x32_bf16 v[78:81], v[146:149], v[178:181], v[78:81]
	v_mfma_f32_16x16x32_bf16 v[74:77], v[154:157], v[178:181], v[74:77]
	v_mfma_f32_16x16x32_bf16 v[70:73], v[146:149], v[186:189], v[70:73]
	v_mfma_f32_16x16x32_bf16 v[66:69], v[154:157], v[186:189], v[66:69]
	v_mfma_f32_16x16x32_bf16 v[94:97], v[150:153], v[166:169], v[94:97]
	v_mfma_f32_16x16x32_bf16 v[90:93], v[158:161], v[166:169], v[90:93]
	v_mfma_f32_16x16x32_bf16 v[86:89], v[150:153], v[174:177], v[86:89]
	v_mfma_f32_16x16x32_bf16 v[82:85], v[158:161], v[174:177], v[82:85]
	v_mfma_f32_16x16x32_bf16 v[78:81], v[150:153], v[182:185], v[78:81]
	v_mfma_f32_16x16x32_bf16 v[74:77], v[158:161], v[182:185], v[74:77]
	v_mfma_f32_16x16x32_bf16 v[70:73], v[150:153], v[190:193], v[70:73]
	v_mfma_f32_16x16x32_bf16 v[66:69], v[158:161], v[190:193], v[66:69]
	s_setprio 0
	s_barrier
	s_add_i32 s46, s48, s53
	v_lshl_add_u64 v[218:219], v[218:219], 0, s[4:5]
	s_mov_b32 m0, s46
	ds_read_b128 v[162:165], v220 offset:49152
	ds_read_b128 v[166:169], v220 offset:50176
	ds_read_b128 v[170:173], v220 offset:51200
	ds_read_b128 v[174:177], v220 offset:52224
	ds_read_b128 v[178:181], v220 offset:53248
	ds_read_b128 v[182:185], v220 offset:54272
	ds_read_b128 v[186:189], v220 offset:55296
	ds_read_b128 v[190:193], v220 offset:56320
	global_load_lds_dwordx4 v[218:219], off
	s_add_i32 m0, s46, 0x2000
	s_add_u32 s44, s44, 0x40080
	v_lshl_add_u64 v[216:217], v[216:217], 0, s[4:5]
	s_addc_u32 s45, s45, 0
	s_add_i32 s46, s49, s53
	global_load_lds_dwordx4 v[216:217], off
	v_lshl_add_u64 v[216:217], s[44:45], 0, v[198:199]
	s_mov_b32 m0, s46
	v_lshl_add_u64 v[212:213], v[212:213], 0, s[4:5]
	global_load_lds_dwordx4 v[216:217], off
	v_lshl_add_u64 v[216:217], s[44:45], 0, v[194:195]
	s_add_i32 m0, s46, 0x2000
	s_nop 0
	global_load_lds_dwordx4 v[216:217], off
	s_mov_b32 m0, s62
	s_nop 0
	global_load_lds_dwordx4 v[212:213], off
	v_lshl_add_u64 v[212:213], v[214:215], 0, s[4:5]
	s_mov_b32 m0, s63
	s_nop 0
	global_load_lds_dwordx4 v[212:213], off
	s_waitcnt vmcnt(8)
	s_waitcnt lgkmcnt(0)
	s_barrier
	s_setprio 1
	s_waitcnt lgkmcnt(0)
	v_mfma_f32_16x16x32_bf16 v[62:65], v[130:133], v[162:165], v[62:65]
	v_mfma_f32_16x16x32_bf16 v[58:61], v[138:141], v[162:165], v[58:61]
	v_mfma_f32_16x16x32_bf16 v[54:57], v[130:133], v[170:173], v[54:57]
	v_mfma_f32_16x16x32_bf16 v[50:53], v[138:141], v[170:173], v[50:53]
	v_mfma_f32_16x16x32_bf16 v[46:49], v[130:133], v[178:181], v[46:49]
	v_mfma_f32_16x16x32_bf16 v[42:45], v[138:141], v[178:181], v[42:45]
	v_mfma_f32_16x16x32_bf16 v[38:41], v[130:133], v[186:189], v[38:41]
	v_mfma_f32_16x16x32_bf16 v[34:37], v[138:141], v[186:189], v[34:37]
	v_mfma_f32_16x16x32_bf16 v[62:65], v[134:137], v[166:169], v[62:65]
	v_mfma_f32_16x16x32_bf16 v[58:61], v[142:145], v[166:169], v[58:61]
	v_mfma_f32_16x16x32_bf16 v[54:57], v[134:137], v[174:177], v[54:57]
	v_mfma_f32_16x16x32_bf16 v[50:53], v[142:145], v[174:177], v[50:53]
	v_mfma_f32_16x16x32_bf16 v[46:49], v[134:137], v[182:185], v[46:49]
	v_mfma_f32_16x16x32_bf16 v[42:45], v[142:145], v[182:185], v[42:45]
	v_mfma_f32_16x16x32_bf16 v[38:41], v[134:137], v[190:193], v[38:41]
	v_mfma_f32_16x16x32_bf16 v[34:37], v[142:145], v[190:193], v[34:37]
	v_mfma_f32_16x16x32_bf16 v[30:33], v[146:149], v[162:165], v[30:33]
	v_mfma_f32_16x16x32_bf16 v[26:29], v[154:157], v[162:165], v[26:29]
	v_mfma_f32_16x16x32_bf16 v[22:25], v[146:149], v[170:173], v[22:25]
	v_mfma_f32_16x16x32_bf16 v[18:21], v[154:157], v[170:173], v[18:21]
	v_mfma_f32_16x16x32_bf16 v[14:17], v[146:149], v[178:181], v[14:17]
	v_mfma_f32_16x16x32_bf16 v[10:13], v[154:157], v[178:181], v[10:13]
	v_mfma_f32_16x16x32_bf16 v[6:9], v[146:149], v[186:189], v[6:9]
	v_mfma_f32_16x16x32_bf16 v[2:5], v[154:157], v[186:189], v[2:5]
	v_mfma_f32_16x16x32_bf16 v[30:33], v[150:153], v[166:169], v[30:33]
	v_mfma_f32_16x16x32_bf16 v[26:29], v[158:161], v[166:169], v[26:29]
	v_mfma_f32_16x16x32_bf16 v[22:25], v[150:153], v[174:177], v[22:25]
	v_mfma_f32_16x16x32_bf16 v[18:21], v[158:161], v[174:177], v[18:21]
	v_mfma_f32_16x16x32_bf16 v[14:17], v[150:153], v[182:185], v[14:17]
	v_mfma_f32_16x16x32_bf16 v[10:13], v[158:161], v[182:185], v[10:13]
	v_mfma_f32_16x16x32_bf16 v[6:9], v[150:153], v[190:193], v[6:9]
	v_mfma_f32_16x16x32_bf16 v[2:5], v[158:161], v[190:193], v[2:5]
	s_setprio 0
	s_barrier
	s_add_i32 s73, s73, 2
	s_add_u32 s42, s42, 0x100
	s_addc_u32 s43, s43, 0
	s_cmp_gt_u32 s73, 13
	s_cbranch_scc1 .LBB0_845
.LBB0_837:
	v_add_u32_e32 v130, 0, v203
	v_add_u32_e32 v131, 0x10000, v130
	v_add_u32_e32 v142, 0x14000, v130
	ds_read_b128 v[146:149], v131
	ds_read_b128 v[150:153], v131 offset:1024
	ds_read_b128 v[154:157], v131 offset:2048
	ds_read_b128 v[158:161], v131 offset:3072
	ds_read_b128 v[130:133], v142
	ds_read_b128 v[134:137], v142 offset:1024
	ds_read_b128 v[138:141], v142 offset:2048
	ds_read_b128 v[142:145], v142 offset:3072
	v_lshl_add_u64 v[212:213], v[208:209], 0, s[42:43]
	s_add_i32 m0, s35, 0xc000
	ds_read_b128 v[186:189], v220
	ds_read_b128 v[190:193], v220 offset:1024
	ds_read_b128 v[178:181], v220 offset:2048
	ds_read_b128 v[182:185], v220 offset:3072
	ds_read_b128 v[170:173], v220 offset:4096
	ds_read_b128 v[174:177], v220 offset:5120
	ds_read_b128 v[162:165], v220 offset:6144
	ds_read_b128 v[166:169], v220 offset:7168
	global_load_lds_dwordx4 v[212:213], off
	v_lshl_add_u64 v[212:213], v[210:211], 0, s[42:43]
	s_add_i32 m0, s35, 0xe000
	s_cmp_lg_u32 s42, 0
	global_load_lds_dwordx4 v[212:213], off
	s_waitcnt vmcnt(8)
	s_waitcnt lgkmcnt(0)
	s_cselect_b64 s[48:49], -1, 0
	s_barrier
	s_setprio 1
	s_and_b64 vcc, exec, s[48:49]
	s_cbranch_vccz .LBB0_842
	s_waitcnt lgkmcnt(0)
	v_mfma_f32_16x16x32_bf16 v[126:129], v[146:149], v[186:189], v[126:129]
	v_mfma_f32_16x16x32_bf16 v[122:125], v[154:157], v[186:189], v[122:125]
	v_mfma_f32_16x16x32_bf16 v[118:121], v[146:149], v[178:181], v[118:121]
	v_mfma_f32_16x16x32_bf16 v[114:117], v[154:157], v[178:181], v[114:117]
	v_mfma_f32_16x16x32_bf16 v[110:113], v[146:149], v[170:173], v[110:113]
	v_mfma_f32_16x16x32_bf16 v[106:109], v[154:157], v[170:173], v[106:109]
	v_mfma_f32_16x16x32_bf16 v[102:105], v[146:149], v[162:165], v[102:105]
	v_mfma_f32_16x16x32_bf16 v[98:101], v[154:157], v[162:165], v[98:101]
	v_mfma_f32_16x16x32_bf16 v[126:129], v[150:153], v[190:193], v[126:129]
	v_mfma_f32_16x16x32_bf16 v[122:125], v[158:161], v[190:193], v[122:125]
	v_mfma_f32_16x16x32_bf16 v[118:121], v[150:153], v[182:185], v[118:121]
	v_mfma_f32_16x16x32_bf16 v[114:117], v[158:161], v[182:185], v[114:117]
	v_mfma_f32_16x16x32_bf16 v[110:113], v[150:153], v[174:177], v[110:113]
	v_mfma_f32_16x16x32_bf16 v[106:109], v[158:161], v[174:177], v[106:109]
	v_mfma_f32_16x16x32_bf16 v[102:105], v[150:153], v[166:169], v[102:105]
	v_mfma_f32_16x16x32_bf16 v[98:101], v[158:161], v[166:169], v[98:101]
	v_mfma_f32_16x16x32_bf16 v[94:97], v[130:133], v[186:189], v[94:97]
	v_mfma_f32_16x16x32_bf16 v[90:93], v[138:141], v[186:189], v[90:93]
	v_mfma_f32_16x16x32_bf16 v[86:89], v[130:133], v[178:181], v[86:89]
	v_mfma_f32_16x16x32_bf16 v[82:85], v[138:141], v[178:181], v[82:85]
	v_mfma_f32_16x16x32_bf16 v[78:81], v[130:133], v[170:173], v[78:81]
	v_mfma_f32_16x16x32_bf16 v[74:77], v[138:141], v[170:173], v[74:77]
	v_mfma_f32_16x16x32_bf16 v[70:73], v[130:133], v[162:165], v[70:73]
	v_mfma_f32_16x16x32_bf16 v[66:69], v[138:141], v[162:165], v[66:69]
	v_mfma_f32_16x16x32_bf16 v[94:97], v[134:137], v[190:193], v[94:97]
	v_mfma_f32_16x16x32_bf16 v[90:93], v[142:145], v[190:193], v[90:93]
	v_mfma_f32_16x16x32_bf16 v[86:89], v[134:137], v[182:185], v[86:89]
	v_mfma_f32_16x16x32_bf16 v[82:85], v[142:145], v[182:185], v[82:85]
	v_mfma_f32_16x16x32_bf16 v[78:81], v[134:137], v[174:177], v[78:81]
	v_mfma_f32_16x16x32_bf16 v[74:77], v[142:145], v[174:177], v[74:77]
	v_mfma_f32_16x16x32_bf16 v[70:73], v[134:137], v[166:169], v[70:73]
	v_mfma_f32_16x16x32_bf16 v[66:69], v[142:145], v[166:169], v[66:69]
	s_cbranch_execnz .LBB0_840

.LBB0_840:
	s_add_u32 s44, s40, s42
	s_addc_u32 s45, s41, s43
	s_add_u32 s44, s44, 0x100
	s_addc_u32 s45, s45, 0
	s_add_u32 s74, s71, s42
	s_addc_u32 s75, s72, s43
	s_cmpk_eq_i32 s42, 0x700
	s_cselect_b32 s47, s25, s45
	s_cselect_b32 s46, s69, s44
	s_cselect_b32 s45, s23, s75
	s_cselect_b32 s44, s70, s74
	s_setprio 0
	s_barrier
	s_mov_b32 m0, s39
	v_lshl_add_u64 v[218:219], s[44:45], 0, v[198:199]
	s_add_u32 s74, s44, 0x40000
	s_waitcnt lgkmcnt(0)
	ds_read_b128 v[186:189], v220 offset:16384
	ds_read_b128 v[190:193], v220 offset:17408
	ds_read_b128 v[178:181], v220 offset:18432
	ds_read_b128 v[182:185], v220 offset:19456
	ds_read_b128 v[170:173], v220 offset:20480
	ds_read_b128 v[174:177], v220 offset:21504
	ds_read_b128 v[162:165], v220 offset:22528
	ds_read_b128 v[166:169], v220 offset:23552
	global_load_lds_dwordx4 v[218:219], off
	v_lshl_add_u64 v[216:217], s[44:45], 0, v[194:195]
	s_mov_b32 m0, s54
	s_addc_u32 s75, s45, 0
	global_load_lds_dwordx4 v[216:217], off
	v_lshl_add_u64 v[212:213], s[74:75], 0, v[198:199]
	s_mov_b32 m0, s55
	v_lshl_add_u64 v[214:215], s[46:47], 0, v[196:197]
	global_load_lds_dwordx4 v[212:213], off
	v_lshl_add_u64 v[212:213], s[74:75], 0, v[194:195]
	s_mov_b32 m0, s56
	s_nop 0
	global_load_lds_dwordx4 v[212:213], off
	v_lshl_add_u64 v[212:213], s[46:47], 0, v[200:201]
	s_mov_b32 m0, s35
	s_nop 0
	global_load_lds_dwordx4 v[212:213], off
	s_mov_b32 m0, s57
	s_nop 0
	global_load_lds_dwordx4 v[214:215], off
	s_waitcnt vmcnt(8)
	s_waitcnt lgkmcnt(0)
	s_barrier
	s_setprio 1
	s_and_b64 vcc, exec, s[48:49]
	s_cbranch_vccz .LBB0_843
	s_waitcnt lgkmcnt(0)
	v_mfma_f32_16x16x32_bf16 v[62:65], v[146:149], v[186:189], v[62:65]
	v_mfma_f32_16x16x32_bf16 v[58:61], v[154:157], v[186:189], v[58:61]
	v_mfma_f32_16x16x32_bf16 v[54:57], v[146:149], v[178:181], v[54:57]
	v_mfma_f32_16x16x32_bf16 v[50:53], v[154:157], v[178:181], v[50:53]
	v_mfma_f32_16x16x32_bf16 v[46:49], v[146:149], v[170:173], v[46:49]
	v_mfma_f32_16x16x32_bf16 v[42:45], v[154:157], v[170:173], v[42:45]
	v_mfma_f32_16x16x32_bf16 v[38:41], v[146:149], v[162:165], v[38:41]
	v_mfma_f32_16x16x32_bf16 v[34:37], v[154:157], v[162:165], v[34:37]
	v_mfma_f32_16x16x32_bf16 v[62:65], v[150:153], v[190:193], v[62:65]
	v_mfma_f32_16x16x32_bf16 v[58:61], v[158:161], v[190:193], v[58:61]
	v_mfma_f32_16x16x32_bf16 v[54:57], v[150:153], v[182:185], v[54:57]
	v_mfma_f32_16x16x32_bf16 v[50:53], v[158:161], v[182:185], v[50:53]
	v_mfma_f32_16x16x32_bf16 v[46:49], v[150:153], v[174:177], v[46:49]
	v_mfma_f32_16x16x32_bf16 v[42:45], v[158:161], v[174:177], v[42:45]
	v_mfma_f32_16x16x32_bf16 v[38:41], v[150:153], v[166:169], v[38:41]
	v_mfma_f32_16x16x32_bf16 v[34:37], v[158:161], v[166:169], v[34:37]
	v_mfma_f32_16x16x32_bf16 v[30:33], v[130:133], v[186:189], v[30:33]
	v_mfma_f32_16x16x32_bf16 v[26:29], v[138:141], v[186:189], v[26:29]
	v_mfma_f32_16x16x32_bf16 v[22:25], v[130:133], v[178:181], v[22:25]
	v_mfma_f32_16x16x32_bf16 v[18:21], v[138:141], v[178:181], v[18:21]
	v_mfma_f32_16x16x32_bf16 v[14:17], v[130:133], v[170:173], v[14:17]
	v_mfma_f32_16x16x32_bf16 v[10:13], v[138:141], v[170:173], v[10:13]
	v_mfma_f32_16x16x32_bf16 v[6:9], v[130:133], v[162:165], v[6:9]
	v_mfma_f32_16x16x32_bf16 v[2:5], v[138:141], v[162:165], v[2:5]
	v_mfma_f32_16x16x32_bf16 v[30:33], v[134:137], v[190:193], v[30:33]
	v_mfma_f32_16x16x32_bf16 v[26:29], v[142:145], v[190:193], v[26:29]
	v_mfma_f32_16x16x32_bf16 v[22:25], v[134:137], v[182:185], v[22:25]
	v_mfma_f32_16x16x32_bf16 v[18:21], v[142:145], v[182:185], v[18:21]
	v_mfma_f32_16x16x32_bf16 v[14:17], v[134:137], v[174:177], v[14:17]
	v_mfma_f32_16x16x32_bf16 v[10:13], v[142:145], v[174:177], v[10:13]
	v_mfma_f32_16x16x32_bf16 v[6:9], v[134:137], v[166:169], v[6:9]
	v_mfma_f32_16x16x32_bf16 v[2:5], v[142:145], v[166:169], v[2:5]
	s_cbranch_execnz .LBB0_836
	s_branch .LBB0_844

.LBB0_1090:
	s_waitcnt lgkmcnt(0)
	s_barrier
	s_setprio 1
	s_mov_b64 s[42:43], -1
	s_and_b64 vcc, exec, s[40:41]
	s_cbranch_vccz .LBB0_1092
	s_waitcnt lgkmcnt(0)
	v_mfma_scale_f32_16x16x128_f8f6f4 v[102:105], v[26:33], v[58:65], v[102:105], v235, v236 op_sel_hi:[0,0,0]
	v_mfma_scale_f32_16x16x128_f8f6f4 v[110:113], v[18:25], v[58:65], v[110:113], v235, v236 op_sel_hi:[0,0,0]
	v_mfma_scale_f32_16x16x128_f8f6f4 v[122:125], v[26:33], v[50:57], v[122:125], v235, v236 op_sel_hi:[0,0,0]
	v_mfma_scale_f32_16x16x128_f8f6f4 v[130:133], v[18:25], v[50:57], v[130:133], v235, v236 op_sel_hi:[0,0,0]
	v_mfma_scale_f32_16x16x128_f8f6f4 v[142:145], v[26:33], v[42:49], v[142:145], v235, v236 op_sel_hi:[0,0,0]
	v_mfma_scale_f32_16x16x128_f8f6f4 v[150:153], v[18:25], v[42:49], v[150:153], v235, v236 op_sel_hi:[0,0,0]
	v_mfma_scale_f32_16x16x128_f8f6f4 v[154:157], v[26:33], v[34:41], v[154:157], v235, v236 op_sel_hi:[0,0,0]
	v_mfma_scale_f32_16x16x128_f8f6f4 v[158:161], v[18:25], v[34:41], v[158:161], v235, v236 op_sel_hi:[0,0,0]
	v_mfma_scale_f32_16x16x128_f8f6f4 v[162:165], v[10:17], v[58:65], v[162:165], v235, v236 op_sel_hi:[0,0,0]
	v_mfma_scale_f32_16x16x128_f8f6f4 v[166:169], v[2:9], v[58:65], v[166:169], v235, v236 op_sel_hi:[0,0,0]
	v_mfma_scale_f32_16x16x128_f8f6f4 v[170:173], v[10:17], v[50:57], v[170:173], v235, v236 op_sel_hi:[0,0,0]
	v_mfma_scale_f32_16x16x128_f8f6f4 v[174:177], v[2:9], v[50:57], v[174:177], v235, v236 op_sel_hi:[0,0,0]
	v_mfma_scale_f32_16x16x128_f8f6f4 v[178:181], v[10:17], v[42:49], v[178:181], v235, v236 op_sel_hi:[0,0,0]
	v_mfma_scale_f32_16x16x128_f8f6f4 v[182:185], v[2:9], v[42:49], v[182:185], v235, v236 op_sel_hi:[0,0,0]
	v_mfma_scale_f32_16x16x128_f8f6f4 v[186:189], v[10:17], v[34:41], v[186:189], v235, v236 op_sel_hi:[0,0,0]
	v_mfma_scale_f32_16x16x128_f8f6f4 v[190:193], v[2:9], v[34:41], v[190:193], v235, v236 op_sel_hi:[0,0,0]
	s_mov_b64 s[42:43], 0
.LBB0_1092:
	s_andn2_b64 vcc, exec, s[42:43]
	s_cbranch_vccnz .LBB0_1094
	s_waitcnt lgkmcnt(0)
	v_mfma_scale_f32_16x16x128_f8f6f4 v[102:105], v[26:33], v[58:65], 0, v235, v236 op_sel_hi:[0,0,0]
	v_mfma_scale_f32_16x16x128_f8f6f4 v[110:113], v[18:25], v[58:65], 0, v235, v236 op_sel_hi:[0,0,0]
	v_mfma_scale_f32_16x16x128_f8f6f4 v[122:125], v[26:33], v[50:57], 0, v235, v236 op_sel_hi:[0,0,0]
	v_mfma_scale_f32_16x16x128_f8f6f4 v[130:133], v[18:25], v[50:57], 0, v235, v236 op_sel_hi:[0,0,0]
	v_mfma_scale_f32_16x16x128_f8f6f4 v[142:145], v[26:33], v[42:49], 0, v235, v236 op_sel_hi:[0,0,0]
	v_mfma_scale_f32_16x16x128_f8f6f4 v[150:153], v[18:25], v[42:49], 0, v235, v236 op_sel_hi:[0,0,0]
	v_mfma_scale_f32_16x16x128_f8f6f4 v[154:157], v[26:33], v[34:41], 0, v235, v236 op_sel_hi:[0,0,0]
	v_mfma_scale_f32_16x16x128_f8f6f4 v[158:161], v[18:25], v[34:41], 0, v235, v236 op_sel_hi:[0,0,0]
	v_mfma_scale_f32_16x16x128_f8f6f4 v[162:165], v[10:17], v[58:65], 0, v235, v236 op_sel_hi:[0,0,0]
	v_mfma_scale_f32_16x16x128_f8f6f4 v[166:169], v[2:9], v[58:65], 0, v235, v236 op_sel_hi:[0,0,0]
	v_mfma_scale_f32_16x16x128_f8f6f4 v[170:173], v[10:17], v[50:57], 0, v235, v236 op_sel_hi:[0,0,0]
	v_mfma_scale_f32_16x16x128_f8f6f4 v[174:177], v[2:9], v[50:57], 0, v235, v236 op_sel_hi:[0,0,0]
	v_mfma_scale_f32_16x16x128_f8f6f4 v[178:181], v[10:17], v[42:49], 0, v235, v236 op_sel_hi:[0,0,0]
	v_mfma_scale_f32_16x16x128_f8f6f4 v[182:185], v[2:9], v[42:49], 0, v235, v236 op_sel_hi:[0,0,0]
	v_mfma_scale_f32_16x16x128_f8f6f4 v[186:189], v[10:17], v[34:41], 0, v235, v236 op_sel_hi:[0,0,0]
	v_mfma_scale_f32_16x16x128_f8f6f4 v[190:193], v[2:9], v[34:41], 0, v235, v236 op_sel_hi:[0,0,0]

.LBB0_1098:
	s_waitcnt lgkmcnt(0)
	s_barrier
	s_setprio 1
	s_mov_b64 s[48:49], -1
	s_and_b64 vcc, exec, s[40:41]
	s_cbranch_vccz .LBB0_1100
	s_waitcnt lgkmcnt(0)
	v_mfma_scale_f32_16x16x128_f8f6f4 v[66:69], v[26:33], v[58:65], v[66:69], v235, v236 op_sel_hi:[0,0,0]
	v_mfma_scale_f32_16x16x128_f8f6f4 v[70:73], v[18:25], v[58:65], v[70:73], v235, v236 op_sel_hi:[0,0,0]
	v_mfma_scale_f32_16x16x128_f8f6f4 v[74:77], v[26:33], v[50:57], v[74:77], v235, v236 op_sel_hi:[0,0,0]
	v_mfma_scale_f32_16x16x128_f8f6f4 v[78:81], v[18:25], v[50:57], v[78:81], v235, v236 op_sel_hi:[0,0,0]
	v_mfma_scale_f32_16x16x128_f8f6f4 v[82:85], v[26:33], v[42:49], v[82:85], v235, v236 op_sel_hi:[0,0,0]
	v_mfma_scale_f32_16x16x128_f8f6f4 v[86:89], v[18:25], v[42:49], v[86:89], v235, v236 op_sel_hi:[0,0,0]
	v_mfma_scale_f32_16x16x128_f8f6f4 v[90:93], v[26:33], v[34:41], v[90:93], v235, v236 op_sel_hi:[0,0,0]
	v_mfma_scale_f32_16x16x128_f8f6f4 v[94:97], v[18:25], v[34:41], v[94:97], v235, v236 op_sel_hi:[0,0,0]
	v_mfma_scale_f32_16x16x128_f8f6f4 v[98:101], v[10:17], v[58:65], v[98:101], v235, v236 op_sel_hi:[0,0,0]
	v_mfma_scale_f32_16x16x128_f8f6f4 v[106:109], v[2:9], v[58:65], v[106:109], v235, v236 op_sel_hi:[0,0,0]
	v_mfma_scale_f32_16x16x128_f8f6f4 v[114:117], v[10:17], v[50:57], v[114:117], v235, v236 op_sel_hi:[0,0,0]
	v_mfma_scale_f32_16x16x128_f8f6f4 v[118:121], v[2:9], v[50:57], v[118:121], v235, v236 op_sel_hi:[0,0,0]
	v_mfma_scale_f32_16x16x128_f8f6f4 v[126:129], v[10:17], v[42:49], v[126:129], v235, v236 op_sel_hi:[0,0,0]
	v_mfma_scale_f32_16x16x128_f8f6f4 v[134:137], v[2:9], v[42:49], v[134:137], v235, v236 op_sel_hi:[0,0,0]
	v_mfma_scale_f32_16x16x128_f8f6f4 v[138:141], v[10:17], v[34:41], v[138:141], v235, v236 op_sel_hi:[0,0,0]
	v_mfma_scale_f32_16x16x128_f8f6f4 v[146:149], v[2:9], v[34:41], v[146:149], v235, v236 op_sel_hi:[0,0,0]
	s_mov_b64 s[48:49], 0
.LBB0_1100:
	s_andn2_b64 vcc, exec, s[48:49]
	s_cbranch_vccnz .LBB0_1102
	s_waitcnt lgkmcnt(0)
	v_mfma_scale_f32_16x16x128_f8f6f4 v[66:69], v[26:33], v[58:65], 0, v235, v236 op_sel_hi:[0,0,0]
	v_mfma_scale_f32_16x16x128_f8f6f4 v[70:73], v[18:25], v[58:65], 0, v235, v236 op_sel_hi:[0,0,0]
	v_mfma_scale_f32_16x16x128_f8f6f4 v[74:77], v[26:33], v[50:57], 0, v235, v236 op_sel_hi:[0,0,0]
	v_mfma_scale_f32_16x16x128_f8f6f4 v[78:81], v[18:25], v[50:57], 0, v235, v236 op_sel_hi:[0,0,0]
	v_mfma_scale_f32_16x16x128_f8f6f4 v[82:85], v[26:33], v[42:49], 0, v235, v236 op_sel_hi:[0,0,0]
	v_mfma_scale_f32_16x16x128_f8f6f4 v[86:89], v[18:25], v[42:49], 0, v235, v236 op_sel_hi:[0,0,0]
	v_mfma_scale_f32_16x16x128_f8f6f4 v[90:93], v[26:33], v[34:41], 0, v235, v236 op_sel_hi:[0,0,0]
	v_mfma_scale_f32_16x16x128_f8f6f4 v[94:97], v[18:25], v[34:41], 0, v235, v236 op_sel_hi:[0,0,0]
	v_mfma_scale_f32_16x16x128_f8f6f4 v[98:101], v[10:17], v[58:65], 0, v235, v236 op_sel_hi:[0,0,0]
	v_mfma_scale_f32_16x16x128_f8f6f4 v[106:109], v[2:9], v[58:65], 0, v235, v236 op_sel_hi:[0,0,0]
	v_mfma_scale_f32_16x16x128_f8f6f4 v[114:117], v[10:17], v[50:57], 0, v235, v236 op_sel_hi:[0,0,0]
	v_mfma_scale_f32_16x16x128_f8f6f4 v[118:121], v[2:9], v[50:57], 0, v235, v236 op_sel_hi:[0,0,0]
	v_mfma_scale_f32_16x16x128_f8f6f4 v[126:129], v[10:17], v[42:49], 0, v235, v236 op_sel_hi:[0,0,0]
	v_mfma_scale_f32_16x16x128_f8f6f4 v[134:137], v[2:9], v[42:49], 0, v235, v236 op_sel_hi:[0,0,0]
	v_mfma_scale_f32_16x16x128_f8f6f4 v[138:141], v[10:17], v[34:41], 0, v235, v236 op_sel_hi:[0,0,0]
	v_mfma_scale_f32_16x16x128_f8f6f4 v[146:149], v[2:9], v[34:41], 0, v235, v236 op_sel_hi:[0,0,0]

.LBB0_1110:
	s_waitcnt lgkmcnt(0)
	v_mov_b32_e32 v227, v199
	v_lshl_add_u64 v[226:227], s[44:45], 0, v[226:227]
	s_barrier
	s_setprio 1
	s_waitcnt lgkmcnt(0)
	v_mfma_scale_f32_16x16x128_f8f6f4 v[102:105], v[26:33], v[58:65], v[102:105], v235, v236 op_sel_hi:[0,0,0]
	v_mfma_scale_f32_16x16x128_f8f6f4 v[110:113], v[18:25], v[58:65], v[110:113], v235, v236 op_sel_hi:[0,0,0]
	v_mfma_scale_f32_16x16x128_f8f6f4 v[122:125], v[26:33], v[50:57], v[122:125], v235, v236 op_sel_hi:[0,0,0]
	v_mfma_scale_f32_16x16x128_f8f6f4 v[130:133], v[18:25], v[50:57], v[130:133], v235, v236 op_sel_hi:[0,0,0]
	v_mfma_scale_f32_16x16x128_f8f6f4 v[142:145], v[26:33], v[42:49], v[142:145], v235, v236 op_sel_hi:[0,0,0]
	v_mfma_scale_f32_16x16x128_f8f6f4 v[150:153], v[18:25], v[42:49], v[150:153], v235, v236 op_sel_hi:[0,0,0]
	v_mfma_scale_f32_16x16x128_f8f6f4 v[154:157], v[26:33], v[34:41], v[154:157], v235, v236 op_sel_hi:[0,0,0]
	v_mfma_scale_f32_16x16x128_f8f6f4 v[158:161], v[18:25], v[34:41], v[158:161], v235, v236 op_sel_hi:[0,0,0]
	v_mfma_scale_f32_16x16x128_f8f6f4 v[162:165], v[10:17], v[58:65], v[162:165], v235, v236 op_sel_hi:[0,0,0]
	v_mfma_scale_f32_16x16x128_f8f6f4 v[166:169], v[2:9], v[58:65], v[166:169], v235, v236 op_sel_hi:[0,0,0]
	v_mfma_scale_f32_16x16x128_f8f6f4 v[170:173], v[10:17], v[50:57], v[170:173], v235, v236 op_sel_hi:[0,0,0]
	v_mfma_scale_f32_16x16x128_f8f6f4 v[174:177], v[2:9], v[50:57], v[174:177], v235, v236 op_sel_hi:[0,0,0]
	v_mfma_scale_f32_16x16x128_f8f6f4 v[178:181], v[10:17], v[42:49], v[178:181], v235, v236 op_sel_hi:[0,0,0]
	v_mfma_scale_f32_16x16x128_f8f6f4 v[182:185], v[2:9], v[42:49], v[182:185], v235, v236 op_sel_hi:[0,0,0]
	v_mfma_scale_f32_16x16x128_f8f6f4 v[186:189], v[10:17], v[34:41], v[186:189], v235, v236 op_sel_hi:[0,0,0]
	v_mfma_scale_f32_16x16x128_f8f6f4 v[190:193], v[2:9], v[34:41], v[190:193], v235, v236 op_sel_hi:[0,0,0]
	s_setprio 0
	s_barrier
	s_mov_b32 m0, s60
	v_lshl_add_u64 v[220:221], v[220:221], 0, s[10:11]
	s_add_u32 s38, s38, 0x20080
	ds_read_b128 v[34:37], v238 offset:49152
	ds_read_b128 v[38:41], v238 offset:50176
	ds_read_b128 v[42:45], v238 offset:51200
	ds_read_b128 v[46:49], v238 offset:52224
	ds_read_b128 v[50:53], v238 offset:53248
	ds_read_b128 v[54:57], v238 offset:54272
	ds_read_b128 v[58:61], v238 offset:55296
	ds_read_b128 v[62:65], v238 offset:56320
	global_load_lds_dwordx4 v[220:221], off
	v_lshl_add_u64 v[220:221], v[222:223], 0, s[10:11]
	s_mov_b32 m0, s61
	s_addc_u32 s39, s39, 0
	global_load_lds_dwordx4 v[220:221], off
	v_lshl_add_u64 v[220:221], s[38:39], 0, v[194:195]
	s_mov_b32 m0, s64
	s_nop 0
	global_load_lds_dwordx4 v[220:221], off
	v_lshl_add_u64 v[220:221], s[38:39], 0, v[196:197]
	s_mov_b32 m0, s65
	s_nop 0
	global_load_lds_dwordx4 v[220:221], off
	v_lshl_add_u64 v[220:221], v[224:225], 0, s[10:11]
	s_mov_b32 m0, s62
	s_nop 0
	global_load_lds_dwordx4 v[220:221], off
	v_lshl_add_u64 v[220:221], v[226:227], 0, s[10:11]
	s_mov_b32 m0, s63
	s_nop 0
	global_load_lds_dwordx4 v[220:221], off
	s_waitcnt vmcnt(8)
	s_waitcnt lgkmcnt(0)
	s_barrier
	s_setprio 1
	s_waitcnt lgkmcnt(0)
	v_mfma_scale_f32_16x16x128_f8f6f4 v[66:69], v[26:33], v[34:41], v[66:69], v235, v236 op_sel_hi:[0,0,0]
	v_mfma_scale_f32_16x16x128_f8f6f4 v[70:73], v[18:25], v[34:41], v[70:73], v235, v236 op_sel_hi:[0,0,0]
	v_mfma_scale_f32_16x16x128_f8f6f4 v[74:77], v[26:33], v[42:49], v[74:77], v235, v236 op_sel_hi:[0,0,0]
	v_mfma_scale_f32_16x16x128_f8f6f4 v[78:81], v[18:25], v[42:49], v[78:81], v235, v236 op_sel_hi:[0,0,0]
	v_mfma_scale_f32_16x16x128_f8f6f4 v[82:85], v[26:33], v[50:57], v[82:85], v235, v236 op_sel_hi:[0,0,0]
	v_mfma_scale_f32_16x16x128_f8f6f4 v[86:89], v[18:25], v[50:57], v[86:89], v235, v236 op_sel_hi:[0,0,0]
	v_mfma_scale_f32_16x16x128_f8f6f4 v[90:93], v[26:33], v[58:65], v[90:93], v235, v236 op_sel_hi:[0,0,0]
	v_mfma_scale_f32_16x16x128_f8f6f4 v[94:97], v[18:25], v[58:65], v[94:97], v235, v236 op_sel_hi:[0,0,0]
	v_mfma_scale_f32_16x16x128_f8f6f4 v[98:101], v[10:17], v[34:41], v[98:101], v235, v236 op_sel_hi:[0,0,0]
	v_mfma_scale_f32_16x16x128_f8f6f4 v[106:109], v[2:9], v[34:41], v[106:109], v235, v236 op_sel_hi:[0,0,0]
	v_mfma_scale_f32_16x16x128_f8f6f4 v[114:117], v[10:17], v[42:49], v[114:117], v235, v236 op_sel_hi:[0,0,0]
	v_mfma_scale_f32_16x16x128_f8f6f4 v[118:121], v[2:9], v[42:49], v[118:121], v235, v236 op_sel_hi:[0,0,0]
	v_mfma_scale_f32_16x16x128_f8f6f4 v[126:129], v[10:17], v[50:57], v[126:129], v235, v236 op_sel_hi:[0,0,0]
	v_mfma_scale_f32_16x16x128_f8f6f4 v[134:137], v[2:9], v[50:57], v[134:137], v235, v236 op_sel_hi:[0,0,0]
	v_mfma_scale_f32_16x16x128_f8f6f4 v[138:141], v[10:17], v[58:65], v[138:141], v235, v236 op_sel_hi:[0,0,0]
	v_mfma_scale_f32_16x16x128_f8f6f4 v[146:149], v[2:9], v[58:65], v[146:149], v235, v236 op_sel_hi:[0,0,0]
	s_setprio 0
	s_barrier
	s_add_i32 s71, s71, 2
	s_cmp_lt_u32 s71, 6
	s_cbranch_scc0 .LBB0_1112
	s_mov_b64 s[38:39], s[36:37]
	s_branch .LBB0_1084

.LBB0_1207:
	s_waitcnt lgkmcnt(0)
	s_barrier
	s_setprio 1
	s_waitcnt lgkmcnt(0)
	v_mfma_scale_f32_16x16x128_f8f6f4 v[102:105], v[26:33], v[58:65], v[102:105], v226, v227 op_sel_hi:[0,0,0]
	v_mfma_scale_f32_16x16x128_f8f6f4 v[110:113], v[18:25], v[58:65], v[110:113], v226, v227 op_sel_hi:[0,0,0]
	v_mfma_scale_f32_16x16x128_f8f6f4 v[122:125], v[26:33], v[50:57], v[122:125], v226, v227 op_sel_hi:[0,0,0]
	v_mfma_scale_f32_16x16x128_f8f6f4 v[130:133], v[18:25], v[50:57], v[130:133], v226, v227 op_sel_hi:[0,0,0]
	v_mfma_scale_f32_16x16x128_f8f6f4 v[142:145], v[26:33], v[42:49], v[142:145], v226, v227 op_sel_hi:[0,0,0]
	v_mfma_scale_f32_16x16x128_f8f6f4 v[150:153], v[18:25], v[42:49], v[150:153], v226, v227 op_sel_hi:[0,0,0]
	v_mfma_scale_f32_16x16x128_f8f6f4 v[154:157], v[26:33], v[34:41], v[154:157], v226, v227 op_sel_hi:[0,0,0]
	v_mfma_scale_f32_16x16x128_f8f6f4 v[158:161], v[18:25], v[34:41], v[158:161], v226, v227 op_sel_hi:[0,0,0]
	v_mfma_scale_f32_16x16x128_f8f6f4 v[162:165], v[10:17], v[58:65], v[162:165], v226, v227 op_sel_hi:[0,0,0]
	v_mfma_scale_f32_16x16x128_f8f6f4 v[166:169], v[2:9], v[58:65], v[166:169], v226, v227 op_sel_hi:[0,0,0]
	v_mfma_scale_f32_16x16x128_f8f6f4 v[170:173], v[10:17], v[50:57], v[170:173], v226, v227 op_sel_hi:[0,0,0]
	v_mfma_scale_f32_16x16x128_f8f6f4 v[174:177], v[2:9], v[50:57], v[174:177], v226, v227 op_sel_hi:[0,0,0]
	v_mfma_scale_f32_16x16x128_f8f6f4 v[178:181], v[10:17], v[42:49], v[178:181], v226, v227 op_sel_hi:[0,0,0]
	v_mfma_scale_f32_16x16x128_f8f6f4 v[182:185], v[2:9], v[42:49], v[182:185], v226, v227 op_sel_hi:[0,0,0]
	v_mfma_scale_f32_16x16x128_f8f6f4 v[186:189], v[10:17], v[34:41], v[186:189], v226, v227 op_sel_hi:[0,0,0]
	v_mfma_scale_f32_16x16x128_f8f6f4 v[190:193], v[2:9], v[34:41], v[190:193], v226, v227 op_sel_hi:[0,0,0]
	s_setprio 0
	s_barrier
	s_mov_b32 m0, s53
	v_lshl_add_u64 v[214:215], v[214:215], 0, s[8:9]
	s_add_u32 s26, s26, 0x20080
	ds_read_b128 v[34:37], v229 offset:49152
	ds_read_b128 v[38:41], v229 offset:50176
	ds_read_b128 v[42:45], v229 offset:51200
	ds_read_b128 v[46:49], v229 offset:52224
	ds_read_b128 v[50:53], v229 offset:53248
	ds_read_b128 v[54:57], v229 offset:54272
	ds_read_b128 v[58:61], v229 offset:55296
	ds_read_b128 v[62:65], v229 offset:56320
	global_load_lds_dwordx4 v[214:215], off
	v_lshl_add_u64 v[214:215], v[216:217], 0, s[8:9]
	s_mov_b32 m0, s54
	s_addc_u32 s27, s27, 0
	global_load_lds_dwordx4 v[214:215], off
	v_lshl_add_u64 v[214:215], s[26:27], 0, v[196:197]
	s_mov_b32 m0, s57
	s_nop 0
	global_load_lds_dwordx4 v[214:215], off
	v_lshl_add_u64 v[214:215], s[26:27], 0, v[200:201]
	s_mov_b32 m0, s58
	s_nop 0
	global_load_lds_dwordx4 v[214:215], off
	v_lshl_add_u64 v[214:215], v[218:219], 0, s[8:9]
	s_mov_b32 m0, s55
	s_nop 0
	global_load_lds_dwordx4 v[214:215], off
	v_lshl_add_u64 v[214:215], v[220:221], 0, s[8:9]
	s_mov_b32 m0, s56
	s_nop 0
	global_load_lds_dwordx4 v[214:215], off
	s_waitcnt vmcnt(8)
	s_waitcnt lgkmcnt(0)
	s_barrier
	s_setprio 1
	s_waitcnt lgkmcnt(0)
	v_mfma_scale_f32_16x16x128_f8f6f4 v[66:69], v[26:33], v[34:41], v[66:69], v226, v227 op_sel_hi:[0,0,0]
	v_mfma_scale_f32_16x16x128_f8f6f4 v[70:73], v[18:25], v[34:41], v[70:73], v226, v227 op_sel_hi:[0,0,0]
	v_mfma_scale_f32_16x16x128_f8f6f4 v[74:77], v[26:33], v[42:49], v[74:77], v226, v227 op_sel_hi:[0,0,0]
	v_mfma_scale_f32_16x16x128_f8f6f4 v[78:81], v[18:25], v[42:49], v[78:81], v226, v227 op_sel_hi:[0,0,0]
	v_mfma_scale_f32_16x16x128_f8f6f4 v[82:85], v[26:33], v[50:57], v[82:85], v226, v227 op_sel_hi:[0,0,0]
	v_mfma_scale_f32_16x16x128_f8f6f4 v[86:89], v[18:25], v[50:57], v[86:89], v226, v227 op_sel_hi:[0,0,0]
	v_mfma_scale_f32_16x16x128_f8f6f4 v[90:93], v[26:33], v[58:65], v[90:93], v226, v227 op_sel_hi:[0,0,0]
	v_mfma_scale_f32_16x16x128_f8f6f4 v[94:97], v[18:25], v[58:65], v[94:97], v226, v227 op_sel_hi:[0,0,0]
	v_mfma_scale_f32_16x16x128_f8f6f4 v[98:101], v[10:17], v[34:41], v[98:101], v226, v227 op_sel_hi:[0,0,0]
	v_mfma_scale_f32_16x16x128_f8f6f4 v[106:109], v[2:9], v[34:41], v[106:109], v226, v227 op_sel_hi:[0,0,0]
	v_mfma_scale_f32_16x16x128_f8f6f4 v[114:117], v[10:17], v[42:49], v[114:117], v226, v227 op_sel_hi:[0,0,0]
	v_mfma_scale_f32_16x16x128_f8f6f4 v[118:121], v[2:9], v[42:49], v[118:121], v226, v227 op_sel_hi:[0,0,0]
	v_mfma_scale_f32_16x16x128_f8f6f4 v[126:129], v[10:17], v[50:57], v[126:129], v226, v227 op_sel_hi:[0,0,0]
	v_mfma_scale_f32_16x16x128_f8f6f4 v[134:137], v[2:9], v[50:57], v[134:137], v226, v227 op_sel_hi:[0,0,0]
	v_mfma_scale_f32_16x16x128_f8f6f4 v[138:141], v[10:17], v[58:65], v[138:141], v226, v227 op_sel_hi:[0,0,0]
	v_mfma_scale_f32_16x16x128_f8f6f4 v[146:149], v[2:9], v[58:65], v[146:149], v226, v227 op_sel_hi:[0,0,0]
	s_setprio 0
	s_barrier
	s_add_i32 s71, s71, 2
	s_add_u32 s24, s24, 0x100
	s_addc_u32 s25, s25, 0
	s_cmp_gt_u32 s71, 5
	s_cbranch_scc1 .LBB0_1228

.LBB0_1212:
	s_waitcnt lgkmcnt(0)
	s_barrier
	s_setprio 1
	s_mov_b64 s[30:31], -1
	s_and_b64 vcc, exec, s[28:29]
	s_cbranch_vccz .LBB0_1214
	s_waitcnt lgkmcnt(0)
	v_mfma_scale_f32_16x16x128_f8f6f4 v[102:105], v[26:33], v[58:65], v[102:105], v226, v227 op_sel_hi:[0,0,0]
	v_mfma_scale_f32_16x16x128_f8f6f4 v[110:113], v[18:25], v[58:65], v[110:113], v226, v227 op_sel_hi:[0,0,0]
	v_mfma_scale_f32_16x16x128_f8f6f4 v[122:125], v[26:33], v[50:57], v[122:125], v226, v227 op_sel_hi:[0,0,0]
	v_mfma_scale_f32_16x16x128_f8f6f4 v[130:133], v[18:25], v[50:57], v[130:133], v226, v227 op_sel_hi:[0,0,0]
	v_mfma_scale_f32_16x16x128_f8f6f4 v[142:145], v[26:33], v[42:49], v[142:145], v226, v227 op_sel_hi:[0,0,0]
	v_mfma_scale_f32_16x16x128_f8f6f4 v[150:153], v[18:25], v[42:49], v[150:153], v226, v227 op_sel_hi:[0,0,0]
	v_mfma_scale_f32_16x16x128_f8f6f4 v[154:157], v[26:33], v[34:41], v[154:157], v226, v227 op_sel_hi:[0,0,0]
	v_mfma_scale_f32_16x16x128_f8f6f4 v[158:161], v[18:25], v[34:41], v[158:161], v226, v227 op_sel_hi:[0,0,0]
	v_mfma_scale_f32_16x16x128_f8f6f4 v[162:165], v[10:17], v[58:65], v[162:165], v226, v227 op_sel_hi:[0,0,0]
	v_mfma_scale_f32_16x16x128_f8f6f4 v[166:169], v[2:9], v[58:65], v[166:169], v226, v227 op_sel_hi:[0,0,0]
	v_mfma_scale_f32_16x16x128_f8f6f4 v[170:173], v[10:17], v[50:57], v[170:173], v226, v227 op_sel_hi:[0,0,0]
	v_mfma_scale_f32_16x16x128_f8f6f4 v[174:177], v[2:9], v[50:57], v[174:177], v226, v227 op_sel_hi:[0,0,0]
	v_mfma_scale_f32_16x16x128_f8f6f4 v[178:181], v[10:17], v[42:49], v[178:181], v226, v227 op_sel_hi:[0,0,0]
	v_mfma_scale_f32_16x16x128_f8f6f4 v[182:185], v[2:9], v[42:49], v[182:185], v226, v227 op_sel_hi:[0,0,0]
	v_mfma_scale_f32_16x16x128_f8f6f4 v[186:189], v[10:17], v[34:41], v[186:189], v226, v227 op_sel_hi:[0,0,0]
	v_mfma_scale_f32_16x16x128_f8f6f4 v[190:193], v[2:9], v[34:41], v[190:193], v226, v227 op_sel_hi:[0,0,0]
	s_mov_b64 s[30:31], 0
.LBB0_1214:
	s_andn2_b64 vcc, exec, s[30:31]
	s_cbranch_vccnz .LBB0_1216
	s_waitcnt lgkmcnt(0)
	v_mfma_scale_f32_16x16x128_f8f6f4 v[102:105], v[26:33], v[58:65], 0, v226, v227 op_sel_hi:[0,0,0]
	v_mfma_scale_f32_16x16x128_f8f6f4 v[110:113], v[18:25], v[58:65], 0, v226, v227 op_sel_hi:[0,0,0]
	v_mfma_scale_f32_16x16x128_f8f6f4 v[122:125], v[26:33], v[50:57], 0, v226, v227 op_sel_hi:[0,0,0]
	v_mfma_scale_f32_16x16x128_f8f6f4 v[130:133], v[18:25], v[50:57], 0, v226, v227 op_sel_hi:[0,0,0]
	v_mfma_scale_f32_16x16x128_f8f6f4 v[142:145], v[26:33], v[42:49], 0, v226, v227 op_sel_hi:[0,0,0]
	v_mfma_scale_f32_16x16x128_f8f6f4 v[150:153], v[18:25], v[42:49], 0, v226, v227 op_sel_hi:[0,0,0]
	v_mfma_scale_f32_16x16x128_f8f6f4 v[154:157], v[26:33], v[34:41], 0, v226, v227 op_sel_hi:[0,0,0]
	v_mfma_scale_f32_16x16x128_f8f6f4 v[158:161], v[18:25], v[34:41], 0, v226, v227 op_sel_hi:[0,0,0]
	v_mfma_scale_f32_16x16x128_f8f6f4 v[162:165], v[10:17], v[58:65], 0, v226, v227 op_sel_hi:[0,0,0]
	v_mfma_scale_f32_16x16x128_f8f6f4 v[166:169], v[2:9], v[58:65], 0, v226, v227 op_sel_hi:[0,0,0]
	v_mfma_scale_f32_16x16x128_f8f6f4 v[170:173], v[10:17], v[50:57], 0, v226, v227 op_sel_hi:[0,0,0]
	v_mfma_scale_f32_16x16x128_f8f6f4 v[174:177], v[2:9], v[50:57], 0, v226, v227 op_sel_hi:[0,0,0]
	v_mfma_scale_f32_16x16x128_f8f6f4 v[178:181], v[10:17], v[42:49], 0, v226, v227 op_sel_hi:[0,0,0]
	v_mfma_scale_f32_16x16x128_f8f6f4 v[182:185], v[2:9], v[42:49], 0, v226, v227 op_sel_hi:[0,0,0]
	v_mfma_scale_f32_16x16x128_f8f6f4 v[186:189], v[10:17], v[34:41], 0, v226, v227 op_sel_hi:[0,0,0]
	v_mfma_scale_f32_16x16x128_f8f6f4 v[190:193], v[2:9], v[34:41], 0, v226, v227 op_sel_hi:[0,0,0]

.LBB0_1220:
	s_waitcnt lgkmcnt(0)
	s_barrier
	s_setprio 1
	s_mov_b64 s[36:37], -1
	s_and_b64 vcc, exec, s[28:29]
	s_cbranch_vccz .LBB0_1222
	s_waitcnt lgkmcnt(0)
	v_mfma_scale_f32_16x16x128_f8f6f4 v[66:69], v[26:33], v[58:65], v[66:69], v226, v227 op_sel_hi:[0,0,0]
	v_mfma_scale_f32_16x16x128_f8f6f4 v[70:73], v[18:25], v[58:65], v[70:73], v226, v227 op_sel_hi:[0,0,0]
	v_mfma_scale_f32_16x16x128_f8f6f4 v[74:77], v[26:33], v[50:57], v[74:77], v226, v227 op_sel_hi:[0,0,0]
	v_mfma_scale_f32_16x16x128_f8f6f4 v[78:81], v[18:25], v[50:57], v[78:81], v226, v227 op_sel_hi:[0,0,0]
	v_mfma_scale_f32_16x16x128_f8f6f4 v[82:85], v[26:33], v[42:49], v[82:85], v226, v227 op_sel_hi:[0,0,0]
	v_mfma_scale_f32_16x16x128_f8f6f4 v[86:89], v[18:25], v[42:49], v[86:89], v226, v227 op_sel_hi:[0,0,0]
	v_mfma_scale_f32_16x16x128_f8f6f4 v[90:93], v[26:33], v[34:41], v[90:93], v226, v227 op_sel_hi:[0,0,0]
	v_mfma_scale_f32_16x16x128_f8f6f4 v[94:97], v[18:25], v[34:41], v[94:97], v226, v227 op_sel_hi:[0,0,0]
	v_mfma_scale_f32_16x16x128_f8f6f4 v[98:101], v[10:17], v[58:65], v[98:101], v226, v227 op_sel_hi:[0,0,0]
	v_mfma_scale_f32_16x16x128_f8f6f4 v[106:109], v[2:9], v[58:65], v[106:109], v226, v227 op_sel_hi:[0,0,0]
	v_mfma_scale_f32_16x16x128_f8f6f4 v[114:117], v[10:17], v[50:57], v[114:117], v226, v227 op_sel_hi:[0,0,0]
	v_mfma_scale_f32_16x16x128_f8f6f4 v[118:121], v[2:9], v[50:57], v[118:121], v226, v227 op_sel_hi:[0,0,0]
	v_mfma_scale_f32_16x16x128_f8f6f4 v[126:129], v[10:17], v[42:49], v[126:129], v226, v227 op_sel_hi:[0,0,0]
	v_mfma_scale_f32_16x16x128_f8f6f4 v[134:137], v[2:9], v[42:49], v[134:137], v226, v227 op_sel_hi:[0,0,0]
	v_mfma_scale_f32_16x16x128_f8f6f4 v[138:141], v[10:17], v[34:41], v[138:141], v226, v227 op_sel_hi:[0,0,0]
	v_mfma_scale_f32_16x16x128_f8f6f4 v[146:149], v[2:9], v[34:41], v[146:149], v226, v227 op_sel_hi:[0,0,0]
	s_mov_b64 s[36:37], 0
.LBB0_1222:
	s_andn2_b64 vcc, exec, s[36:37]
	s_cbranch_vccnz .LBB0_1224
	s_waitcnt lgkmcnt(0)
	v_mfma_scale_f32_16x16x128_f8f6f4 v[66:69], v[26:33], v[58:65], 0, v226, v227 op_sel_hi:[0,0,0]
	v_mfma_scale_f32_16x16x128_f8f6f4 v[70:73], v[18:25], v[58:65], 0, v226, v227 op_sel_hi:[0,0,0]
	v_mfma_scale_f32_16x16x128_f8f6f4 v[74:77], v[26:33], v[50:57], 0, v226, v227 op_sel_hi:[0,0,0]
	v_mfma_scale_f32_16x16x128_f8f6f4 v[78:81], v[18:25], v[50:57], 0, v226, v227 op_sel_hi:[0,0,0]
	v_mfma_scale_f32_16x16x128_f8f6f4 v[82:85], v[26:33], v[42:49], 0, v226, v227 op_sel_hi:[0,0,0]
	v_mfma_scale_f32_16x16x128_f8f6f4 v[86:89], v[18:25], v[42:49], 0, v226, v227 op_sel_hi:[0,0,0]
	v_mfma_scale_f32_16x16x128_f8f6f4 v[90:93], v[26:33], v[34:41], 0, v226, v227 op_sel_hi:[0,0,0]
	v_mfma_scale_f32_16x16x128_f8f6f4 v[94:97], v[18:25], v[34:41], 0, v226, v227 op_sel_hi:[0,0,0]
	v_mfma_scale_f32_16x16x128_f8f6f4 v[98:101], v[10:17], v[58:65], 0, v226, v227 op_sel_hi:[0,0,0]
	v_mfma_scale_f32_16x16x128_f8f6f4 v[106:109], v[2:9], v[58:65], 0, v226, v227 op_sel_hi:[0,0,0]
	v_mfma_scale_f32_16x16x128_f8f6f4 v[114:117], v[10:17], v[50:57], 0, v226, v227 op_sel_hi:[0,0,0]
	v_mfma_scale_f32_16x16x128_f8f6f4 v[118:121], v[2:9], v[50:57], 0, v226, v227 op_sel_hi:[0,0,0]
	v_mfma_scale_f32_16x16x128_f8f6f4 v[126:129], v[10:17], v[42:49], 0, v226, v227 op_sel_hi:[0,0,0]
	v_mfma_scale_f32_16x16x128_f8f6f4 v[134:137], v[2:9], v[42:49], 0, v226, v227 op_sel_hi:[0,0,0]
	v_mfma_scale_f32_16x16x128_f8f6f4 v[138:141], v[10:17], v[34:41], 0, v226, v227 op_sel_hi:[0,0,0]
	v_mfma_scale_f32_16x16x128_f8f6f4 v[146:149], v[2:9], v[34:41], 0, v226, v227 op_sel_hi:[0,0,0]
